# v6
# speedup vs baseline: 1.0718x; 1.0009x over previous
.Lnerf_hid_a0:
	s_waitcnt vmcnt(0) lgkmcnt(0)
	s_barrier
	ds_read_b128 v[224:227], v121 offset:40960
	ds_read_b128 v[228:231], v121 offset:41984
	v_mfma_f32_16x16x32_bf16 v[80:83], v[240:243], v[208:211], v[80:83]
	ds_read_b128 v[232:235], v121 offset:43008
	v_mfma_f32_16x16x32_bf16 v[76:79], v[244:247], v[208:211], v[76:79]
	ds_read_b128 v[236:239], v121 offset:44032
	v_mfma_f32_16x16x32_bf16 v[72:75], v[244:247], v[212:215], v[72:75]
	v_mfma_f32_16x16x32_bf16 v[84:87], v[240:243], v[212:215], v[84:87]
	ds_read_b128 v[240:243], v121 offset:45056
	ds_read_b128 v[244:247], v121 offset:46080
	v_mfma_f32_16x16x32_bf16 v[80:83], v[248:251], v[216:219], v[80:83]
	v_mfma_f32_16x16x32_bf16 v[76:79], v[252:255], v[216:219], v[76:79]
	v_mfma_f32_16x16x32_bf16 v[72:75], v[252:255], v[220:223], v[72:75]
	v_mfma_f32_16x16x32_bf16 v[84:87], v[248:251], v[220:223], v[84:87]
	ds_read_b128 v[248:251], v121 offset:47104
	ds_read_b128 v[252:255], v121 offset:48128
	s_setprio 3
	s_waitcnt lgkmcnt(6)
	v_mfma_f32_16x16x32_bf16 v[64:67], v[224:227], v[0:3], v[152:155]
	v_mfma_f32_16x16x32_bf16 v[68:71], v[228:231], v[0:3], v[156:159]
	v_mfma_f32_16x16x32_bf16 v[60:63], v[228:231], v[4:7], v[156:159]
	v_mfma_f32_16x16x32_bf16 v[56:59], v[224:227], v[4:7], v[152:155]
	ds_read_b128 v[224:227], v121 offset:49152
	ds_read_b128 v[228:231], v121 offset:50176
	s_waitcnt lgkmcnt(6)
	ds_read_b128 v[160:163], v183 offset:128
	ds_read_b128 v[164:167], v183 offset:192
	v_mfma_f32_16x16x32_bf16 v[64:67], v[232:235], v[12:15], v[64:67]
	v_mfma_f32_16x16x32_bf16 v[68:71], v[236:239], v[12:15], v[68:71]
	s_mov_b32 m0, s35
	s_add_i32 s51, s50, 0x0
	v_mfma_f32_16x16x32_bf16 v[60:63], v[236:239], v[8:11], v[60:63]
	buffer_load_dwordx4 v125, s[36:39], s51 offen lds
	v_mfma_f32_16x16x32_bf16 v[56:59], v[232:235], v[8:11], v[56:59]
	ds_read_b128 v[232:235], v121 offset:51200
	ds_read_b128 v[236:239], v121 offset:52224
	s_waitcnt lgkmcnt(8)
	v_mfma_f32_16x16x32_bf16 v[64:67], v[240:243], v[16:19], v[64:67]
	v_mfma_f32_16x16x32_bf16 v[68:71], v[244:247], v[16:19], v[68:71]
	s_mov_b32 m0, s42
	s_add_i32 s51, s50, 0x2000
	v_mfma_f32_16x16x32_bf16 v[60:63], v[244:247], v[20:23], v[60:63]
	buffer_load_dwordx4 v125, s[36:39], s51 offen lds
	v_mfma_f32_16x16x32_bf16 v[56:59], v[240:243], v[20:23], v[56:59]
	ds_read_b128 v[240:243], v121 offset:53248
	ds_read_b128 v[244:247], v121 offset:54272
	s_waitcnt lgkmcnt(8)
	v_mfma_f32_16x16x32_bf16 v[64:67], v[248:251], v[24:27], v[64:67]
	v_cvt_pk_bf16_f32 v112, v80, v81
	v_mfma_f32_16x16x32_bf16 v[68:71], v[252:255], v[24:27], v[68:71]
	s_mov_b32 m0, s41
	s_add_i32 s51, s50, 0x4000
	v_cvt_pk_bf16_f32 v113, v82, v83
	v_mfma_f32_16x16x32_bf16 v[60:63], v[252:255], v[28:31], v[60:63]
	buffer_load_dwordx4 v125, s[36:39], s51 offen lds
	v_cvt_pk_bf16_f32 v114, v76, v77
	v_mfma_f32_16x16x32_bf16 v[56:59], v[248:251], v[28:31], v[56:59]
	v_cvt_pk_bf16_f32 v115, v78, v79
	ds_read_b128 v[248:251], v121 offset:55296
	ds_read_b128 v[252:255], v121 offset:56320
	s_setprio 2
	s_waitcnt lgkmcnt(8)
	v_mfma_f32_16x16x32_bf16 v[64:67], v[224:227], v[32:35], v[64:67]
	v_cvt_pk_bf16_f32 v116, v84, v85
	v_mfma_f32_16x16x32_bf16 v[68:71], v[228:231], v[32:35], v[68:71]
	s_mov_b32 m0, s40
	s_add_i32 s51, s50, 0x6000
	v_cvt_pk_bf16_f32 v117, v86, v87
	v_mfma_f32_16x16x32_bf16 v[60:63], v[228:231], v[36:39], v[60:63]
	buffer_load_dwordx4 v125, s[36:39], s51 offen lds
	v_cvt_pk_bf16_f32 v118, v72, v73
	v_mfma_f32_16x16x32_bf16 v[56:59], v[224:227], v[36:39], v[56:59]
	v_cvt_pk_bf16_f32 v119, v74, v75
	ds_read_b128 v[224:227], v121 offset:57344
	ds_read_b128 v[228:231], v121 offset:58368
	s_waitcnt lgkmcnt(6)
	v_mfma_f32_16x16x32_bf16 v[64:67], v[232:235], v[40:43], v[64:67]
	v_pk_max_i16 v112, v112, 0
	v_mfma_f32_16x16x32_bf16 v[68:71], v[236:239], v[40:43], v[68:71]
	v_pk_max_i16 v113, v113, 0
	v_mfma_f32_16x16x32_bf16 v[60:63], v[236:239], v[44:47], v[60:63]
	v_pk_max_i16 v114, v114, 0
	v_mfma_f32_16x16x32_bf16 v[56:59], v[232:235], v[44:47], v[56:59]
	v_pk_max_i16 v115, v115, 0
	ds_read_b128 v[232:235], v121 offset:59392
	ds_read_b128 v[236:239], v121 offset:60416
	s_waitcnt lgkmcnt(6)
	ds_read_b128 v[152:155], v183 offset:256
	ds_read_b128 v[156:159], v183 offset:320
	v_mfma_f32_16x16x32_bf16 v[64:67], v[240:243], v[48:51], v[64:67]
	v_pk_max_i16 v116, v116, 0
	v_mfma_f32_16x16x32_bf16 v[68:71], v[244:247], v[48:51], v[68:71]
	v_pk_max_i16 v117, v117, 0
	v_mfma_f32_16x16x32_bf16 v[60:63], v[244:247], v[52:55], v[60:63]
	v_pk_max_i16 v118, v118, 0
	v_mfma_f32_16x16x32_bf16 v[56:59], v[240:243], v[52:55], v[56:59]
	v_pk_max_i16 v119, v119, 0
	ds_read_b128 v[240:243], v121 offset:61440
	ds_read_b128 v[244:247], v121 offset:62464
	s_waitcnt lgkmcnt(8)
	v_mfma_f32_16x16x32_bf16 v[64:67], v[248:251], v[112:115], v[64:67]
	v_mfma_f32_16x16x32_bf16 v[68:71], v[252:255], v[112:115], v[68:71]
	v_mfma_f32_16x16x32_bf16 v[60:63], v[252:255], v[116:119], v[60:63]
	v_mfma_f32_16x16x32_bf16 v[56:59], v[248:251], v[116:119], v[56:59]
	ds_read_b128 v[248:251], v121 offset:63488
	ds_read_b128 v[252:255], v121 offset:64512
	s_setprio 1
	s_waitcnt lgkmcnt(8)
	v_mfma_f32_16x16x32_bf16 v[80:83], v[224:227], v[0:3], v[160:163]
	v_mfma_f32_16x16x32_bf16 v[76:79], v[228:231], v[0:3], v[164:167]
	v_mfma_f32_16x16x32_bf16 v[72:75], v[228:231], v[4:7], v[164:167]
	v_mfma_f32_16x16x32_bf16 v[84:87], v[224:227], v[4:7], v[160:163]
	ds_read_b128 v[224:227], v126 offset:57344
	ds_read_b128 v[228:231], v126 offset:58368
	s_waitcnt lgkmcnt(8)
	v_mfma_f32_16x16x32_bf16 v[80:83], v[232:235], v[12:15], v[80:83]
	v_cvt_pk_bf16_f32 v88, v64, v65
	v_mfma_f32_16x16x32_bf16 v[76:79], v[236:239], v[12:15], v[76:79]
	v_cvt_pk_bf16_f32 v89, v66, v67
	v_mfma_f32_16x16x32_bf16 v[72:75], v[236:239], v[8:11], v[72:75]
	v_cvt_pk_bf16_f32 v90, v68, v69
	v_mfma_f32_16x16x32_bf16 v[84:87], v[232:235], v[8:11], v[84:87]
	v_cvt_pk_bf16_f32 v91, v70, v71
	ds_read_b128 v[232:235], v126 offset:59392
	ds_read_b128 v[236:239], v126 offset:60416
	s_waitcnt lgkmcnt(6)
	v_mfma_f32_16x16x32_bf16 v[80:83], v[240:243], v[16:19], v[80:83]
	v_cvt_pk_bf16_f32 v92, v56, v57
	v_mfma_f32_16x16x32_bf16 v[76:79], v[244:247], v[16:19], v[76:79]
	v_cvt_pk_bf16_f32 v93, v58, v59
	v_mfma_f32_16x16x32_bf16 v[72:75], v[244:247], v[20:23], v[72:75]
	v_cvt_pk_bf16_f32 v94, v60, v61
	v_mfma_f32_16x16x32_bf16 v[84:87], v[240:243], v[20:23], v[84:87]
	v_cvt_pk_bf16_f32 v95, v62, v63
	ds_read_b128 v[240:243], v126 offset:61440
	ds_read_b128 v[244:247], v126 offset:62464
	s_waitcnt lgkmcnt(6)
	v_mfma_f32_16x16x32_bf16 v[80:83], v[248:251], v[24:27], v[80:83]
	v_pk_max_i16 v88, v88, 0
	v_mfma_f32_16x16x32_bf16 v[76:79], v[252:255], v[24:27], v[76:79]
	v_pk_max_i16 v89, v89, 0
	v_mfma_f32_16x16x32_bf16 v[72:75], v[252:255], v[28:31], v[72:75]
	v_pk_max_i16 v90, v90, 0
	v_mfma_f32_16x16x32_bf16 v[84:87], v[248:251], v[28:31], v[84:87]
	v_pk_max_i16 v91, v91, 0
	ds_read_b128 v[248:251], v126 offset:63488
	ds_read_b128 v[252:255], v126 offset:64512
	s_setprio 0
	s_waitcnt lgkmcnt(6)
	v_mfma_f32_16x16x32_bf16 v[80:83], v[224:227], v[32:35], v[80:83]
	v_pk_max_i16 v92, v92, 0
	v_mfma_f32_16x16x32_bf16 v[76:79], v[228:231], v[32:35], v[76:79]
	v_pk_max_i16 v93, v93, 0
	v_mfma_f32_16x16x32_bf16 v[72:75], v[228:231], v[36:39], v[72:75]
	v_pk_max_i16 v94, v94, 0
	v_mfma_f32_16x16x32_bf16 v[84:87], v[224:227], v[36:39], v[84:87]
	v_pk_max_i16 v95, v95, 0
	s_waitcnt lgkmcnt(4)
	v_mfma_f32_16x16x32_bf16 v[80:83], v[232:235], v[40:43], v[80:83]
	v_mfma_f32_16x16x32_bf16 v[76:79], v[236:239], v[40:43], v[76:79]
	v_mfma_f32_16x16x32_bf16 v[72:75], v[236:239], v[44:47], v[72:75]
	v_mfma_f32_16x16x32_bf16 v[84:87], v[232:235], v[44:47], v[84:87]
.Lnerf_hid_a1:
	s_waitcnt vmcnt(0) lgkmcnt(0)
	s_barrier
	ds_read_b128 v[224:227], v121 offset:8192
	ds_read_b128 v[228:231], v121 offset:9216
	v_mfma_f32_16x16x32_bf16 v[80:83], v[240:243], v[48:51], v[80:83]
	ds_read_b128 v[232:235], v121 offset:10240
	v_mfma_f32_16x16x32_bf16 v[76:79], v[244:247], v[48:51], v[76:79]
	ds_read_b128 v[236:239], v121 offset:11264
	v_mfma_f32_16x16x32_bf16 v[72:75], v[244:247], v[52:55], v[72:75]
	v_mfma_f32_16x16x32_bf16 v[84:87], v[240:243], v[52:55], v[84:87]
	ds_read_b128 v[240:243], v121 offset:12288
	ds_read_b128 v[244:247], v121 offset:13312
	v_mfma_f32_16x16x32_bf16 v[80:83], v[248:251], v[112:115], v[80:83]
	v_mfma_f32_16x16x32_bf16 v[76:79], v[252:255], v[112:115], v[76:79]
	v_mfma_f32_16x16x32_bf16 v[72:75], v[252:255], v[116:119], v[72:75]
	v_mfma_f32_16x16x32_bf16 v[84:87], v[248:251], v[116:119], v[84:87]
	ds_read_b128 v[248:251], v121 offset:14336
	ds_read_b128 v[252:255], v121 offset:15360
	s_setprio 3
	s_waitcnt lgkmcnt(6)
	v_mfma_f32_16x16x32_bf16 v[64:67], v[224:227], v[0:3], v[152:155]
	v_mfma_f32_16x16x32_bf16 v[68:71], v[228:231], v[0:3], v[156:159]
	v_mfma_f32_16x16x32_bf16 v[60:63], v[228:231], v[4:7], v[156:159]
	v_mfma_f32_16x16x32_bf16 v[56:59], v[224:227], v[4:7], v[152:155]
	ds_read_b128 v[224:227], v121 offset:16384
	ds_read_b128 v[228:231], v121 offset:17408
	s_waitcnt lgkmcnt(6)
	ds_read_b128 v[160:163], v183 offset:384
	ds_read_b128 v[164:167], v183 offset:448
	v_mfma_f32_16x16x32_bf16 v[64:67], v[232:235], v[12:15], v[64:67]
	v_mfma_f32_16x16x32_bf16 v[68:71], v[236:239], v[12:15], v[68:71]
	s_mov_b32 m0, s28
	s_add_i32 s51, s50, 0x8000
	v_mfma_f32_16x16x32_bf16 v[60:63], v[236:239], v[8:11], v[60:63]
	buffer_load_dwordx4 v125, s[36:39], s51 offen lds
	v_mfma_f32_16x16x32_bf16 v[56:59], v[232:235], v[8:11], v[56:59]
	ds_read_b128 v[232:235], v121 offset:18432
	ds_read_b128 v[236:239], v121 offset:19456
	s_waitcnt lgkmcnt(8)
	v_mfma_f32_16x16x32_bf16 v[64:67], v[240:243], v[16:19], v[64:67]
	v_mfma_f32_16x16x32_bf16 v[68:71], v[244:247], v[16:19], v[68:71]
	s_mov_b32 m0, s29
	s_add_i32 s51, s50, 0xa000
	v_mfma_f32_16x16x32_bf16 v[60:63], v[244:247], v[20:23], v[60:63]
	buffer_load_dwordx4 v125, s[36:39], s51 offen lds
	v_mfma_f32_16x16x32_bf16 v[56:59], v[240:243], v[20:23], v[56:59]
	ds_read_b128 v[240:243], v121 offset:20480
	ds_read_b128 v[244:247], v121 offset:21504
	s_waitcnt lgkmcnt(8)
	v_mfma_f32_16x16x32_bf16 v[64:67], v[248:251], v[24:27], v[64:67]
	v_mfma_f32_16x16x32_bf16 v[68:71], v[252:255], v[24:27], v[68:71]
	s_mov_b32 m0, s33
	s_add_i32 s51, s50, 0xc000
	v_mfma_f32_16x16x32_bf16 v[60:63], v[252:255], v[28:31], v[60:63]
	buffer_load_dwordx4 v125, s[36:39], s51 offen lds
	v_mfma_f32_16x16x32_bf16 v[56:59], v[248:251], v[28:31], v[56:59]
	ds_read_b128 v[248:251], v121 offset:22528
	ds_read_b128 v[252:255], v121 offset:23552
	s_setprio 2
	s_waitcnt lgkmcnt(8)
	v_mfma_f32_16x16x32_bf16 v[64:67], v[224:227], v[32:35], v[64:67]
	v_mfma_f32_16x16x32_bf16 v[68:71], v[228:231], v[32:35], v[68:71]
	s_mov_b32 m0, s34
	s_add_i32 s51, s50, 0xe000
	v_mfma_f32_16x16x32_bf16 v[60:63], v[228:231], v[36:39], v[60:63]
	buffer_load_dwordx4 v125, s[36:39], s51 offen lds
	v_mfma_f32_16x16x32_bf16 v[56:59], v[224:227], v[36:39], v[56:59]
	ds_read_b128 v[224:227], v121 offset:24576
	ds_read_b128 v[228:231], v121 offset:25600
	s_waitcnt lgkmcnt(6)
	v_mfma_f32_16x16x32_bf16 v[64:67], v[232:235], v[40:43], v[64:67]
	v_cvt_pk_bf16_f32 v96, v80, v81
	v_mfma_f32_16x16x32_bf16 v[68:71], v[236:239], v[40:43], v[68:71]
	v_cvt_pk_bf16_f32 v97, v82, v83
	v_mfma_f32_16x16x32_bf16 v[60:63], v[236:239], v[44:47], v[60:63]
	v_cvt_pk_bf16_f32 v98, v76, v77
	v_mfma_f32_16x16x32_bf16 v[56:59], v[232:235], v[44:47], v[56:59]
	v_cvt_pk_bf16_f32 v99, v78, v79
	ds_read_b128 v[232:235], v121 offset:26624
	ds_read_b128 v[236:239], v121 offset:27648
	s_waitcnt lgkmcnt(6)
	ds_read_b128 v[152:155], v183 offset:512
	ds_read_b128 v[156:159], v183 offset:576
	v_mfma_f32_16x16x32_bf16 v[64:67], v[240:243], v[48:51], v[64:67]
	v_cvt_pk_bf16_f32 v100, v84, v85
	v_mfma_f32_16x16x32_bf16 v[68:71], v[244:247], v[48:51], v[68:71]
	v_cvt_pk_bf16_f32 v101, v86, v87
	v_mfma_f32_16x16x32_bf16 v[60:63], v[244:247], v[52:55], v[60:63]
	v_cvt_pk_bf16_f32 v102, v72, v73
	v_mfma_f32_16x16x32_bf16 v[56:59], v[240:243], v[52:55], v[56:59]
	v_cvt_pk_bf16_f32 v103, v74, v75
	ds_read_b128 v[240:243], v121 offset:28672
	ds_read_b128 v[244:247], v121 offset:29696
	s_waitcnt lgkmcnt(8)
	v_mfma_f32_16x16x32_bf16 v[64:67], v[248:251], v[112:115], v[64:67]
	v_pk_max_i16 v96, v96, 0
	v_mfma_f32_16x16x32_bf16 v[68:71], v[252:255], v[112:115], v[68:71]
	v_pk_max_i16 v97, v97, 0
	v_mfma_f32_16x16x32_bf16 v[60:63], v[252:255], v[116:119], v[60:63]
	v_pk_max_i16 v98, v98, 0
	v_mfma_f32_16x16x32_bf16 v[56:59], v[248:251], v[116:119], v[56:59]
	v_pk_max_i16 v99, v99, 0
	ds_read_b128 v[248:251], v121 offset:30720
	ds_read_b128 v[252:255], v121 offset:31744
	s_setprio 1
	s_waitcnt lgkmcnt(8)
	v_mfma_f32_16x16x32_bf16 v[80:83], v[224:227], v[0:3], v[160:163]
	v_pk_max_i16 v100, v100, 0
	v_mfma_f32_16x16x32_bf16 v[76:79], v[228:231], v[0:3], v[164:167]
	v_pk_max_i16 v101, v101, 0
	v_mfma_f32_16x16x32_bf16 v[72:75], v[228:231], v[4:7], v[164:167]
	v_pk_max_i16 v102, v102, 0
	v_mfma_f32_16x16x32_bf16 v[84:87], v[224:227], v[4:7], v[160:163]
	v_pk_max_i16 v103, v103, 0
	ds_read_b128 v[224:227], v121 offset:32768
	ds_read_b128 v[228:231], v121 offset:33792
	s_waitcnt lgkmcnt(8)
	v_mfma_f32_16x16x32_bf16 v[80:83], v[232:235], v[12:15], v[80:83]
	v_cvt_pk_bf16_f32 v104, v64, v65
	v_mfma_f32_16x16x32_bf16 v[76:79], v[236:239], v[12:15], v[76:79]
	v_cvt_pk_bf16_f32 v105, v66, v67
	v_mfma_f32_16x16x32_bf16 v[72:75], v[236:239], v[8:11], v[72:75]
	v_cvt_pk_bf16_f32 v106, v68, v69
	v_mfma_f32_16x16x32_bf16 v[84:87], v[232:235], v[8:11], v[84:87]
	v_cvt_pk_bf16_f32 v107, v70, v71
	ds_read_b128 v[232:235], v121 offset:34816
	ds_read_b128 v[236:239], v121 offset:35840
	s_waitcnt lgkmcnt(6)
	v_mfma_f32_16x16x32_bf16 v[80:83], v[240:243], v[16:19], v[80:83]
	v_cvt_pk_bf16_f32 v108, v56, v57
	v_mfma_f32_16x16x32_bf16 v[76:79], v[244:247], v[16:19], v[76:79]
	v_cvt_pk_bf16_f32 v109, v58, v59
	v_mfma_f32_16x16x32_bf16 v[72:75], v[244:247], v[20:23], v[72:75]
	v_cvt_pk_bf16_f32 v110, v60, v61
	v_mfma_f32_16x16x32_bf16 v[84:87], v[240:243], v[20:23], v[84:87]
	v_cvt_pk_bf16_f32 v111, v62, v63
	ds_read_b128 v[240:243], v121 offset:36864
	ds_read_b128 v[244:247], v121 offset:37888
	s_waitcnt lgkmcnt(6)
	v_mfma_f32_16x16x32_bf16 v[80:83], v[248:251], v[24:27], v[80:83]
	v_pk_max_i16 v104, v104, 0
	v_mfma_f32_16x16x32_bf16 v[76:79], v[252:255], v[24:27], v[76:79]
	v_pk_max_i16 v105, v105, 0
	v_mfma_f32_16x16x32_bf16 v[72:75], v[252:255], v[28:31], v[72:75]
	v_pk_max_i16 v106, v106, 0
	v_mfma_f32_16x16x32_bf16 v[84:87], v[248:251], v[28:31], v[84:87]
	v_pk_max_i16 v107, v107, 0
	ds_read_b128 v[248:251], v121 offset:38912
	ds_read_b128 v[252:255], v121 offset:39936
	s_setprio 0
	s_waitcnt lgkmcnt(6)
	v_mfma_f32_16x16x32_bf16 v[80:83], v[224:227], v[32:35], v[80:83]
	v_pk_max_i16 v108, v108, 0
	v_mfma_f32_16x16x32_bf16 v[76:79], v[228:231], v[32:35], v[76:79]
	v_pk_max_i16 v109, v109, 0
	v_mfma_f32_16x16x32_bf16 v[72:75], v[228:231], v[36:39], v[72:75]
	v_pk_max_i16 v110, v110, 0
	v_mfma_f32_16x16x32_bf16 v[84:87], v[224:227], v[36:39], v[84:87]
	v_pk_max_i16 v111, v111, 0
	s_waitcnt lgkmcnt(4)
	v_mfma_f32_16x16x32_bf16 v[80:83], v[232:235], v[40:43], v[80:83]
	v_mfma_f32_16x16x32_bf16 v[76:79], v[236:239], v[40:43], v[76:79]
	v_mfma_f32_16x16x32_bf16 v[72:75], v[236:239], v[44:47], v[72:75]
	v_mfma_f32_16x16x32_bf16 v[84:87], v[232:235], v[44:47], v[84:87]
.Lnerf_hid_a2:
	s_waitcnt vmcnt(0) lgkmcnt(0)
	s_barrier
	ds_read_b128 v[224:227], v121 offset:40960
	ds_read_b128 v[228:231], v121 offset:41984
	v_mfma_f32_16x16x32_bf16 v[80:83], v[240:243], v[48:51], v[80:83]
	ds_read_b128 v[232:235], v121 offset:43008
	v_mfma_f32_16x16x32_bf16 v[76:79], v[244:247], v[48:51], v[76:79]
	ds_read_b128 v[236:239], v121 offset:44032
	v_mfma_f32_16x16x32_bf16 v[72:75], v[244:247], v[52:55], v[72:75]
	v_mfma_f32_16x16x32_bf16 v[84:87], v[240:243], v[52:55], v[84:87]
	ds_read_b128 v[240:243], v121 offset:45056
	ds_read_b128 v[244:247], v121 offset:46080
	v_mfma_f32_16x16x32_bf16 v[80:83], v[248:251], v[112:115], v[80:83]
	v_mfma_f32_16x16x32_bf16 v[76:79], v[252:255], v[112:115], v[76:79]
	v_mfma_f32_16x16x32_bf16 v[72:75], v[252:255], v[116:119], v[72:75]
	v_mfma_f32_16x16x32_bf16 v[84:87], v[248:251], v[116:119], v[84:87]
	ds_read_b128 v[248:251], v121 offset:47104
	ds_read_b128 v[252:255], v121 offset:48128
	s_setprio 3
	s_waitcnt lgkmcnt(6)
	v_mfma_f32_16x16x32_bf16 v[64:67], v[224:227], v[0:3], v[152:155]
	v_mfma_f32_16x16x32_bf16 v[68:71], v[228:231], v[0:3], v[156:159]
	v_mfma_f32_16x16x32_bf16 v[60:63], v[228:231], v[4:7], v[156:159]
	v_mfma_f32_16x16x32_bf16 v[56:59], v[224:227], v[4:7], v[152:155]
	ds_read_b128 v[224:227], v121 offset:49152
	ds_read_b128 v[228:231], v121 offset:50176
	s_waitcnt lgkmcnt(6)
	ds_read_b128 v[160:163], v183 offset:640
	ds_read_b128 v[164:167], v183 offset:704
	v_mfma_f32_16x16x32_bf16 v[64:67], v[232:235], v[12:15], v[64:67]
	v_mfma_f32_16x16x32_bf16 v[68:71], v[236:239], v[12:15], v[68:71]
	s_mov_b32 m0, s35
	s_add_i32 s51, s50, 0x10000
	v_mfma_f32_16x16x32_bf16 v[60:63], v[236:239], v[8:11], v[60:63]
	buffer_load_dwordx4 v125, s[36:39], s51 offen lds
	v_mfma_f32_16x16x32_bf16 v[56:59], v[232:235], v[8:11], v[56:59]
	ds_read_b128 v[232:235], v121 offset:51200
	ds_read_b128 v[236:239], v121 offset:52224
	s_waitcnt lgkmcnt(8)
	v_mfma_f32_16x16x32_bf16 v[64:67], v[240:243], v[16:19], v[64:67]
	v_mfma_f32_16x16x32_bf16 v[68:71], v[244:247], v[16:19], v[68:71]
	s_mov_b32 m0, s42
	s_add_i32 s51, s50, 0x12000
	v_mfma_f32_16x16x32_bf16 v[60:63], v[244:247], v[20:23], v[60:63]
	buffer_load_dwordx4 v125, s[36:39], s51 offen lds
	v_mfma_f32_16x16x32_bf16 v[56:59], v[240:243], v[20:23], v[56:59]
	ds_read_b128 v[240:243], v121 offset:53248
	ds_read_b128 v[244:247], v121 offset:54272
	s_waitcnt lgkmcnt(8)
	v_mfma_f32_16x16x32_bf16 v[64:67], v[248:251], v[24:27], v[64:67]
	v_mfma_f32_16x16x32_bf16 v[68:71], v[252:255], v[24:27], v[68:71]
	s_mov_b32 m0, s41
	s_add_i32 s51, s50, 0x14000
	v_mfma_f32_16x16x32_bf16 v[60:63], v[252:255], v[28:31], v[60:63]
	buffer_load_dwordx4 v125, s[36:39], s51 offen lds
	v_mfma_f32_16x16x32_bf16 v[56:59], v[248:251], v[28:31], v[56:59]
	ds_read_b128 v[248:251], v121 offset:55296
	ds_read_b128 v[252:255], v121 offset:56320
	s_setprio 2
	s_waitcnt lgkmcnt(8)
	v_mfma_f32_16x16x32_bf16 v[64:67], v[224:227], v[32:35], v[64:67]
	v_mfma_f32_16x16x32_bf16 v[68:71], v[228:231], v[32:35], v[68:71]
	s_mov_b32 m0, s40
	s_add_i32 s51, s50, 0x16000
	v_mfma_f32_16x16x32_bf16 v[60:63], v[228:231], v[36:39], v[60:63]
	buffer_load_dwordx4 v125, s[36:39], s51 offen lds
	v_mfma_f32_16x16x32_bf16 v[56:59], v[224:227], v[36:39], v[56:59]
	ds_read_b128 v[224:227], v121 offset:57344
	ds_read_b128 v[228:231], v121 offset:58368
	s_waitcnt lgkmcnt(6)
	v_mfma_f32_16x16x32_bf16 v[64:67], v[232:235], v[40:43], v[64:67]
	v_cvt_pk_bf16_f32 v184, v80, v81
	v_mfma_f32_16x16x32_bf16 v[68:71], v[236:239], v[40:43], v[68:71]
	v_cvt_pk_bf16_f32 v185, v82, v83
	v_mfma_f32_16x16x32_bf16 v[60:63], v[236:239], v[44:47], v[60:63]
	v_cvt_pk_bf16_f32 v186, v76, v77
	v_mfma_f32_16x16x32_bf16 v[56:59], v[232:235], v[44:47], v[56:59]
	v_cvt_pk_bf16_f32 v187, v78, v79
	ds_read_b128 v[232:235], v121 offset:59392
	ds_read_b128 v[236:239], v121 offset:60416
	s_waitcnt lgkmcnt(6)
	ds_read_b128 v[152:155], v183 offset:768
	ds_read_b128 v[156:159], v183 offset:832
	v_mfma_f32_16x16x32_bf16 v[64:67], v[240:243], v[48:51], v[64:67]
	v_cvt_pk_bf16_f32 v188, v84, v85
	v_mfma_f32_16x16x32_bf16 v[68:71], v[244:247], v[48:51], v[68:71]
	v_cvt_pk_bf16_f32 v189, v86, v87
	v_mfma_f32_16x16x32_bf16 v[60:63], v[244:247], v[52:55], v[60:63]
	v_cvt_pk_bf16_f32 v190, v72, v73
	v_mfma_f32_16x16x32_bf16 v[56:59], v[240:243], v[52:55], v[56:59]
	v_cvt_pk_bf16_f32 v191, v74, v75
	ds_read_b128 v[240:243], v121 offset:61440
	ds_read_b128 v[244:247], v121 offset:62464
	s_waitcnt lgkmcnt(8)
	v_mfma_f32_16x16x32_bf16 v[64:67], v[248:251], v[112:115], v[64:67]
	v_pk_max_i16 v184, v184, 0
	v_mfma_f32_16x16x32_bf16 v[68:71], v[252:255], v[112:115], v[68:71]
	v_pk_max_i16 v185, v185, 0
	v_mfma_f32_16x16x32_bf16 v[60:63], v[252:255], v[116:119], v[60:63]
	v_pk_max_i16 v186, v186, 0
	v_mfma_f32_16x16x32_bf16 v[56:59], v[248:251], v[116:119], v[56:59]
	v_pk_max_i16 v187, v187, 0
	ds_read_b128 v[248:251], v121 offset:63488
	ds_read_b128 v[252:255], v121 offset:64512
	s_setprio 1
	s_waitcnt lgkmcnt(8)
	v_mfma_f32_16x16x32_bf16 v[80:83], v[224:227], v[0:3], v[160:163]
	v_pk_max_i16 v188, v188, 0
	v_mfma_f32_16x16x32_bf16 v[76:79], v[228:231], v[0:3], v[164:167]
	v_pk_max_i16 v189, v189, 0
	v_mfma_f32_16x16x32_bf16 v[72:75], v[228:231], v[4:7], v[164:167]
	v_pk_max_i16 v190, v190, 0
	v_mfma_f32_16x16x32_bf16 v[84:87], v[224:227], v[4:7], v[160:163]
	v_pk_max_i16 v191, v191, 0
	ds_read_b128 v[224:227], v126 offset:57344
	ds_read_b128 v[228:231], v126 offset:58368
	s_waitcnt lgkmcnt(8)
	v_mfma_f32_16x16x32_bf16 v[80:83], v[232:235], v[12:15], v[80:83]
	v_cvt_pk_bf16_f32 v192, v64, v65
	v_mfma_f32_16x16x32_bf16 v[76:79], v[236:239], v[12:15], v[76:79]
	v_cvt_pk_bf16_f32 v193, v66, v67
	v_mfma_f32_16x16x32_bf16 v[72:75], v[236:239], v[8:11], v[72:75]
	v_cvt_pk_bf16_f32 v194, v68, v69
	v_mfma_f32_16x16x32_bf16 v[84:87], v[232:235], v[8:11], v[84:87]
	v_cvt_pk_bf16_f32 v195, v70, v71
	ds_read_b128 v[232:235], v126 offset:59392
	ds_read_b128 v[236:239], v126 offset:60416
	s_waitcnt lgkmcnt(6)
	v_mfma_f32_16x16x32_bf16 v[80:83], v[240:243], v[16:19], v[80:83]
	v_cvt_pk_bf16_f32 v196, v56, v57
	v_mfma_f32_16x16x32_bf16 v[76:79], v[244:247], v[16:19], v[76:79]
	v_cvt_pk_bf16_f32 v197, v58, v59
	v_mfma_f32_16x16x32_bf16 v[72:75], v[244:247], v[20:23], v[72:75]
	v_cvt_pk_bf16_f32 v198, v60, v61
	v_mfma_f32_16x16x32_bf16 v[84:87], v[240:243], v[20:23], v[84:87]
	v_cvt_pk_bf16_f32 v199, v62, v63
	ds_read_b128 v[240:243], v126 offset:61440
	ds_read_b128 v[244:247], v126 offset:62464
	s_waitcnt lgkmcnt(6)
	v_mfma_f32_16x16x32_bf16 v[80:83], v[248:251], v[24:27], v[80:83]
	v_pk_max_i16 v192, v192, 0
	v_mfma_f32_16x16x32_bf16 v[76:79], v[252:255], v[24:27], v[76:79]
	v_pk_max_i16 v193, v193, 0
	v_mfma_f32_16x16x32_bf16 v[72:75], v[252:255], v[28:31], v[72:75]
	v_pk_max_i16 v194, v194, 0
	v_mfma_f32_16x16x32_bf16 v[84:87], v[248:251], v[28:31], v[84:87]
	v_pk_max_i16 v195, v195, 0
	ds_read_b128 v[248:251], v126 offset:63488
	ds_read_b128 v[252:255], v126 offset:64512
	s_setprio 0
	s_waitcnt lgkmcnt(6)
	v_mfma_f32_16x16x32_bf16 v[80:83], v[224:227], v[32:35], v[80:83]
	v_pk_max_i16 v196, v196, 0
	v_mfma_f32_16x16x32_bf16 v[76:79], v[228:231], v[32:35], v[76:79]
	v_pk_max_i16 v197, v197, 0
	v_mfma_f32_16x16x32_bf16 v[72:75], v[228:231], v[36:39], v[72:75]
	v_pk_max_i16 v198, v198, 0
	v_mfma_f32_16x16x32_bf16 v[84:87], v[224:227], v[36:39], v[84:87]
	v_pk_max_i16 v199, v199, 0
	s_waitcnt lgkmcnt(4)
	v_mfma_f32_16x16x32_bf16 v[80:83], v[232:235], v[40:43], v[80:83]
	v_mfma_f32_16x16x32_bf16 v[76:79], v[236:239], v[40:43], v[76:79]
	v_mfma_f32_16x16x32_bf16 v[72:75], v[236:239], v[44:47], v[72:75]
	v_mfma_f32_16x16x32_bf16 v[84:87], v[232:235], v[44:47], v[84:87]
.Lnerf_hid_a3:
	s_waitcnt vmcnt(0) lgkmcnt(0)
	s_barrier
	ds_read_b128 v[224:227], v121 offset:8192
	ds_read_b128 v[228:231], v121 offset:9216
	v_mfma_f32_16x16x32_bf16 v[80:83], v[240:243], v[48:51], v[80:83]
	ds_read_b128 v[232:235], v121 offset:10240
	v_mfma_f32_16x16x32_bf16 v[76:79], v[244:247], v[48:51], v[76:79]
	ds_read_b128 v[236:239], v121 offset:11264
	v_mfma_f32_16x16x32_bf16 v[72:75], v[244:247], v[52:55], v[72:75]
	v_mfma_f32_16x16x32_bf16 v[84:87], v[240:243], v[52:55], v[84:87]
	ds_read_b128 v[240:243], v121 offset:12288
	ds_read_b128 v[244:247], v121 offset:13312
	v_mfma_f32_16x16x32_bf16 v[80:83], v[248:251], v[112:115], v[80:83]
	v_mfma_f32_16x16x32_bf16 v[76:79], v[252:255], v[112:115], v[76:79]
	v_mfma_f32_16x16x32_bf16 v[72:75], v[252:255], v[116:119], v[72:75]
	v_mfma_f32_16x16x32_bf16 v[84:87], v[248:251], v[116:119], v[84:87]
	ds_read_b128 v[248:251], v121 offset:14336
	ds_read_b128 v[252:255], v121 offset:15360
	s_setprio 3
	s_waitcnt lgkmcnt(6)
	v_mfma_f32_16x16x32_bf16 v[64:67], v[224:227], v[0:3], v[152:155]
	v_mfma_f32_16x16x32_bf16 v[68:71], v[228:231], v[0:3], v[156:159]
	v_mfma_f32_16x16x32_bf16 v[60:63], v[228:231], v[4:7], v[156:159]
	v_mfma_f32_16x16x32_bf16 v[56:59], v[224:227], v[4:7], v[152:155]
	ds_read_b128 v[224:227], v121 offset:16384
	ds_read_b128 v[228:231], v121 offset:17408
	s_waitcnt lgkmcnt(6)
	ds_read_b128 v[160:163], v183 offset:896
	ds_read_b128 v[164:167], v183 offset:960
	v_mfma_f32_16x16x32_bf16 v[64:67], v[232:235], v[12:15], v[64:67]
	v_mfma_f32_16x16x32_bf16 v[68:71], v[236:239], v[12:15], v[68:71]
	s_mov_b32 m0, s28
	s_add_i32 s51, s50, 0x18000
	v_mfma_f32_16x16x32_bf16 v[60:63], v[236:239], v[8:11], v[60:63]
	buffer_load_dwordx4 v125, s[36:39], s51 offen lds
	v_mfma_f32_16x16x32_bf16 v[56:59], v[232:235], v[8:11], v[56:59]
	ds_read_b128 v[232:235], v121 offset:18432
	ds_read_b128 v[236:239], v121 offset:19456
	s_waitcnt lgkmcnt(8)
	v_mfma_f32_16x16x32_bf16 v[64:67], v[240:243], v[16:19], v[64:67]
	v_mfma_f32_16x16x32_bf16 v[68:71], v[244:247], v[16:19], v[68:71]
	s_mov_b32 m0, s29
	s_add_i32 s51, s50, 0x1a000
	v_mfma_f32_16x16x32_bf16 v[60:63], v[244:247], v[20:23], v[60:63]
	buffer_load_dwordx4 v125, s[36:39], s51 offen lds
	v_mfma_f32_16x16x32_bf16 v[56:59], v[240:243], v[20:23], v[56:59]
	ds_read_b128 v[240:243], v121 offset:20480
	ds_read_b128 v[244:247], v121 offset:21504
	s_waitcnt lgkmcnt(8)
	v_mfma_f32_16x16x32_bf16 v[64:67], v[248:251], v[24:27], v[64:67]
	v_mfma_f32_16x16x32_bf16 v[68:71], v[252:255], v[24:27], v[68:71]
	s_mov_b32 m0, s33
	s_add_i32 s51, s50, 0x1c000
	v_mfma_f32_16x16x32_bf16 v[60:63], v[252:255], v[28:31], v[60:63]
	buffer_load_dwordx4 v125, s[36:39], s51 offen lds
	v_mfma_f32_16x16x32_bf16 v[56:59], v[248:251], v[28:31], v[56:59]
	ds_read_b128 v[248:251], v121 offset:22528
	ds_read_b128 v[252:255], v121 offset:23552
	s_setprio 2
	s_waitcnt lgkmcnt(8)
	v_mfma_f32_16x16x32_bf16 v[64:67], v[224:227], v[32:35], v[64:67]
	v_mfma_f32_16x16x32_bf16 v[68:71], v[228:231], v[32:35], v[68:71]
	s_mov_b32 m0, s34
	s_add_i32 s51, s50, 0x1e000
	v_mfma_f32_16x16x32_bf16 v[60:63], v[228:231], v[36:39], v[60:63]
	buffer_load_dwordx4 v125, s[36:39], s51 offen lds
	v_mfma_f32_16x16x32_bf16 v[56:59], v[224:227], v[36:39], v[56:59]
	ds_read_b128 v[224:227], v121 offset:24576
	ds_read_b128 v[228:231], v121 offset:25600
	s_waitcnt lgkmcnt(6)
	v_mfma_f32_16x16x32_bf16 v[64:67], v[232:235], v[40:43], v[64:67]
	v_cvt_pk_bf16_f32 v200, v80, v81
	v_mfma_f32_16x16x32_bf16 v[68:71], v[236:239], v[40:43], v[68:71]
	v_cvt_pk_bf16_f32 v201, v82, v83
	v_mfma_f32_16x16x32_bf16 v[60:63], v[236:239], v[44:47], v[60:63]
	v_cvt_pk_bf16_f32 v202, v76, v77
	v_mfma_f32_16x16x32_bf16 v[56:59], v[232:235], v[44:47], v[56:59]
	v_cvt_pk_bf16_f32 v203, v78, v79
	ds_read_b128 v[232:235], v121 offset:26624
	ds_read_b128 v[236:239], v121 offset:27648
	s_waitcnt lgkmcnt(6)
	ds_read_b128 v[152:155], v183 offset:1024
	ds_read_b128 v[156:159], v183 offset:1088
	v_mfma_f32_16x16x32_bf16 v[64:67], v[240:243], v[48:51], v[64:67]
	v_cvt_pk_bf16_f32 v204, v84, v85
	v_mfma_f32_16x16x32_bf16 v[68:71], v[244:247], v[48:51], v[68:71]
	v_cvt_pk_bf16_f32 v205, v86, v87
	v_mfma_f32_16x16x32_bf16 v[60:63], v[244:247], v[52:55], v[60:63]
	v_cvt_pk_bf16_f32 v206, v72, v73
	v_mfma_f32_16x16x32_bf16 v[56:59], v[240:243], v[52:55], v[56:59]
	v_cvt_pk_bf16_f32 v207, v74, v75
	ds_read_b128 v[240:243], v121 offset:28672
	ds_read_b128 v[244:247], v121 offset:29696
	s_waitcnt lgkmcnt(8)
	v_mfma_f32_16x16x32_bf16 v[64:67], v[248:251], v[112:115], v[64:67]
	v_pk_max_i16 v200, v200, 0
	v_mfma_f32_16x16x32_bf16 v[68:71], v[252:255], v[112:115], v[68:71]
	v_pk_max_i16 v201, v201, 0
	v_mfma_f32_16x16x32_bf16 v[60:63], v[252:255], v[116:119], v[60:63]
	v_pk_max_i16 v202, v202, 0
	v_mfma_f32_16x16x32_bf16 v[56:59], v[248:251], v[116:119], v[56:59]
	v_pk_max_i16 v203, v203, 0
	ds_read_b128 v[248:251], v121 offset:30720
	ds_read_b128 v[252:255], v121 offset:31744
	s_setprio 1
	s_waitcnt lgkmcnt(8)
	v_mfma_f32_16x16x32_bf16 v[80:83], v[224:227], v[0:3], v[160:163]
	v_pk_max_i16 v204, v204, 0
	v_mfma_f32_16x16x32_bf16 v[76:79], v[228:231], v[0:3], v[164:167]
	v_pk_max_i16 v205, v205, 0
	v_mfma_f32_16x16x32_bf16 v[72:75], v[228:231], v[4:7], v[164:167]
	v_pk_max_i16 v206, v206, 0
	v_mfma_f32_16x16x32_bf16 v[84:87], v[224:227], v[4:7], v[160:163]
	v_pk_max_i16 v207, v207, 0
	ds_read_b128 v[224:227], v121 offset:32768
	ds_read_b128 v[228:231], v121 offset:33792
	s_waitcnt lgkmcnt(8)
	v_mfma_f32_16x16x32_bf16 v[80:83], v[232:235], v[12:15], v[80:83]
	v_cvt_pk_bf16_f32 v208, v64, v65
	v_mfma_f32_16x16x32_bf16 v[76:79], v[236:239], v[12:15], v[76:79]
	v_cvt_pk_bf16_f32 v209, v66, v67
	v_mfma_f32_16x16x32_bf16 v[72:75], v[236:239], v[8:11], v[72:75]
	v_cvt_pk_bf16_f32 v210, v68, v69
	v_mfma_f32_16x16x32_bf16 v[84:87], v[232:235], v[8:11], v[84:87]
	v_cvt_pk_bf16_f32 v211, v70, v71
	ds_read_b128 v[232:235], v121 offset:34816
	ds_read_b128 v[236:239], v121 offset:35840
	s_waitcnt lgkmcnt(6)
	v_mfma_f32_16x16x32_bf16 v[80:83], v[240:243], v[16:19], v[80:83]
	v_cvt_pk_bf16_f32 v212, v56, v57
	v_mfma_f32_16x16x32_bf16 v[76:79], v[244:247], v[16:19], v[76:79]
	v_cvt_pk_bf16_f32 v213, v58, v59
	v_mfma_f32_16x16x32_bf16 v[72:75], v[244:247], v[20:23], v[72:75]
	v_cvt_pk_bf16_f32 v214, v60, v61
	v_mfma_f32_16x16x32_bf16 v[84:87], v[240:243], v[20:23], v[84:87]
	v_cvt_pk_bf16_f32 v215, v62, v63
	ds_read_b128 v[240:243], v121 offset:36864
	ds_read_b128 v[244:247], v121 offset:37888
	s_waitcnt lgkmcnt(6)
	v_mfma_f32_16x16x32_bf16 v[80:83], v[248:251], v[24:27], v[80:83]
	v_pk_max_i16 v208, v208, 0
	v_mfma_f32_16x16x32_bf16 v[76:79], v[252:255], v[24:27], v[76:79]
	v_pk_max_i16 v209, v209, 0
	v_mfma_f32_16x16x32_bf16 v[72:75], v[252:255], v[28:31], v[72:75]
	v_pk_max_i16 v210, v210, 0
	v_mfma_f32_16x16x32_bf16 v[84:87], v[248:251], v[28:31], v[84:87]
	v_pk_max_i16 v211, v211, 0
	ds_read_b128 v[248:251], v121 offset:38912
	ds_read_b128 v[252:255], v121 offset:39936
	s_setprio 0
	s_waitcnt lgkmcnt(6)
	v_mfma_f32_16x16x32_bf16 v[80:83], v[224:227], v[32:35], v[80:83]
	v_pk_max_i16 v212, v212, 0
	v_mfma_f32_16x16x32_bf16 v[76:79], v[228:231], v[32:35], v[76:79]
	v_pk_max_i16 v213, v213, 0
	v_mfma_f32_16x16x32_bf16 v[72:75], v[228:231], v[36:39], v[72:75]
	v_pk_max_i16 v214, v214, 0
	v_mfma_f32_16x16x32_bf16 v[84:87], v[224:227], v[36:39], v[84:87]
	v_pk_max_i16 v215, v215, 0
	s_waitcnt lgkmcnt(4)
	v_mfma_f32_16x16x32_bf16 v[80:83], v[232:235], v[40:43], v[80:83]
	v_mfma_f32_16x16x32_bf16 v[76:79], v[236:239], v[40:43], v[76:79]
	v_mfma_f32_16x16x32_bf16 v[72:75], v[236:239], v[44:47], v[72:75]
	v_mfma_f32_16x16x32_bf16 v[84:87], v[232:235], v[44:47], v[84:87]
	s_cmp_eq_u32 s52, 3
	s_cbranch_scc1 .Lnerf_head
.Lnerf_hid_a4:
	s_waitcnt vmcnt(0) lgkmcnt(0)
	s_barrier
	ds_read_b128 v[224:227], v121 offset:40960
	ds_read_b128 v[228:231], v121 offset:41984
	v_mfma_f32_16x16x32_bf16 v[80:83], v[240:243], v[48:51], v[80:83]
	ds_read_b128 v[232:235], v121 offset:43008
	v_mfma_f32_16x16x32_bf16 v[76:79], v[244:247], v[48:51], v[76:79]
	ds_read_b128 v[236:239], v121 offset:44032
	v_mfma_f32_16x16x32_bf16 v[72:75], v[244:247], v[52:55], v[72:75]
	v_mfma_f32_16x16x32_bf16 v[84:87], v[240:243], v[52:55], v[84:87]
	ds_read_b128 v[240:243], v121 offset:45056
	ds_read_b128 v[244:247], v121 offset:46080
	v_mfma_f32_16x16x32_bf16 v[80:83], v[248:251], v[112:115], v[80:83]
	v_mfma_f32_16x16x32_bf16 v[76:79], v[252:255], v[112:115], v[76:79]
	v_mfma_f32_16x16x32_bf16 v[72:75], v[252:255], v[116:119], v[72:75]
	v_mfma_f32_16x16x32_bf16 v[84:87], v[248:251], v[116:119], v[84:87]
	ds_read_b128 v[248:251], v121 offset:47104
	ds_read_b128 v[252:255], v121 offset:48128
	s_setprio 3
	s_waitcnt lgkmcnt(6)
	v_mfma_f32_16x16x32_bf16 v[64:67], v[224:227], v[88:91], v[152:155]
	v_mfma_f32_16x16x32_bf16 v[68:71], v[228:231], v[88:91], v[156:159]
	v_mfma_f32_16x16x32_bf16 v[60:63], v[228:231], v[92:95], v[156:159]
	v_mfma_f32_16x16x32_bf16 v[56:59], v[224:227], v[92:95], v[152:155]
	ds_read_b128 v[224:227], v121 offset:49152
	ds_read_b128 v[228:231], v121 offset:50176
	s_waitcnt lgkmcnt(6)
	ds_read_b128 v[160:163], v183 offset:1152
	ds_read_b128 v[164:167], v183 offset:1216
	v_mfma_f32_16x16x32_bf16 v[64:67], v[232:235], v[96:99], v[64:67]
	v_mfma_f32_16x16x32_bf16 v[68:71], v[236:239], v[96:99], v[68:71]
	s_mov_b32 m0, s35
	s_add_i32 s51, s50, 0x20000
	v_mfma_f32_16x16x32_bf16 v[60:63], v[236:239], v[100:103], v[60:63]
	buffer_load_dwordx4 v125, s[36:39], s51 offen lds
	v_mfma_f32_16x16x32_bf16 v[56:59], v[232:235], v[100:103], v[56:59]
	ds_read_b128 v[232:235], v121 offset:51200
	ds_read_b128 v[236:239], v121 offset:52224
	s_waitcnt lgkmcnt(8)
	v_mfma_f32_16x16x32_bf16 v[64:67], v[240:243], v[104:107], v[64:67]
	v_mfma_f32_16x16x32_bf16 v[68:71], v[244:247], v[104:107], v[68:71]
	s_mov_b32 m0, s42
	s_add_i32 s51, s50, 0x22000
	v_mfma_f32_16x16x32_bf16 v[60:63], v[244:247], v[108:111], v[60:63]
	buffer_load_dwordx4 v125, s[36:39], s51 offen lds
	v_mfma_f32_16x16x32_bf16 v[56:59], v[240:243], v[108:111], v[56:59]
	ds_read_b128 v[240:243], v121 offset:53248
	ds_read_b128 v[244:247], v121 offset:54272
	s_waitcnt lgkmcnt(8)
	v_mfma_f32_16x16x32_bf16 v[64:67], v[248:251], v[184:187], v[64:67]
	v_cvt_pk_bf16_f32 v216, v80, v81
	v_mfma_f32_16x16x32_bf16 v[68:71], v[252:255], v[184:187], v[68:71]
	s_mov_b32 m0, s41
	s_add_i32 s51, s50, 0x24000
	v_cvt_pk_bf16_f32 v217, v82, v83
	v_mfma_f32_16x16x32_bf16 v[60:63], v[252:255], v[188:191], v[60:63]
	buffer_load_dwordx4 v125, s[36:39], s51 offen lds
	v_cvt_pk_bf16_f32 v218, v76, v77
	v_mfma_f32_16x16x32_bf16 v[56:59], v[248:251], v[188:191], v[56:59]
	v_cvt_pk_bf16_f32 v219, v78, v79
	ds_read_b128 v[248:251], v121 offset:55296
	ds_read_b128 v[252:255], v121 offset:56320
	s_setprio 2
	s_waitcnt lgkmcnt(8)
	v_mfma_f32_16x16x32_bf16 v[64:67], v[224:227], v[192:195], v[64:67]
	v_cvt_pk_bf16_f32 v220, v84, v85
	v_mfma_f32_16x16x32_bf16 v[68:71], v[228:231], v[192:195], v[68:71]
	s_mov_b32 m0, s40
	s_add_i32 s51, s50, 0x26000
	v_cvt_pk_bf16_f32 v221, v86, v87
	v_mfma_f32_16x16x32_bf16 v[60:63], v[228:231], v[196:199], v[60:63]
	buffer_load_dwordx4 v125, s[36:39], s51 offen lds
	v_cvt_pk_bf16_f32 v222, v72, v73
	v_mfma_f32_16x16x32_bf16 v[56:59], v[224:227], v[196:199], v[56:59]
	v_cvt_pk_bf16_f32 v223, v74, v75
	ds_read_b128 v[224:227], v121 offset:57344
	ds_read_b128 v[228:231], v121 offset:58368
	s_waitcnt lgkmcnt(6)
	v_mfma_f32_16x16x32_bf16 v[64:67], v[232:235], v[200:203], v[64:67]
	v_pk_max_i16 v216, v216, 0
	v_mfma_f32_16x16x32_bf16 v[68:71], v[236:239], v[200:203], v[68:71]
	v_pk_max_i16 v217, v217, 0
	v_mfma_f32_16x16x32_bf16 v[60:63], v[236:239], v[204:207], v[60:63]
	v_pk_max_i16 v218, v218, 0
	v_mfma_f32_16x16x32_bf16 v[56:59], v[232:235], v[204:207], v[56:59]
	v_pk_max_i16 v219, v219, 0
	ds_read_b128 v[232:235], v121 offset:59392
	ds_read_b128 v[236:239], v121 offset:60416
	s_waitcnt lgkmcnt(6)
	ds_read_b128 v[152:155], v183 offset:1280
	ds_read_b128 v[156:159], v183 offset:1344
	v_mfma_f32_16x16x32_bf16 v[64:67], v[240:243], v[208:211], v[64:67]
	v_pk_max_i16 v220, v220, 0
	v_mfma_f32_16x16x32_bf16 v[68:71], v[244:247], v[208:211], v[68:71]
	v_pk_max_i16 v221, v221, 0
	v_mfma_f32_16x16x32_bf16 v[60:63], v[244:247], v[212:215], v[60:63]
	v_pk_max_i16 v222, v222, 0
	v_mfma_f32_16x16x32_bf16 v[56:59], v[240:243], v[212:215], v[56:59]
	v_pk_max_i16 v223, v223, 0
	ds_read_b128 v[240:243], v121 offset:61440
	ds_read_b128 v[244:247], v121 offset:62464
	s_waitcnt lgkmcnt(8)
	v_mfma_f32_16x16x32_bf16 v[64:67], v[248:251], v[216:219], v[64:67]
	v_mfma_f32_16x16x32_bf16 v[68:71], v[252:255], v[216:219], v[68:71]
	v_mfma_f32_16x16x32_bf16 v[60:63], v[252:255], v[220:223], v[60:63]
	v_mfma_f32_16x16x32_bf16 v[56:59], v[248:251], v[220:223], v[56:59]
	ds_read_b128 v[248:251], v121 offset:63488
	ds_read_b128 v[252:255], v121 offset:64512
	s_setprio 1
	s_waitcnt lgkmcnt(8)
	v_mfma_f32_16x16x32_bf16 v[80:83], v[224:227], v[88:91], v[160:163]
	v_mfma_f32_16x16x32_bf16 v[76:79], v[228:231], v[88:91], v[164:167]
	v_mfma_f32_16x16x32_bf16 v[72:75], v[228:231], v[92:95], v[164:167]
	v_mfma_f32_16x16x32_bf16 v[84:87], v[224:227], v[92:95], v[160:163]
	ds_read_b128 v[224:227], v126 offset:57344
	ds_read_b128 v[228:231], v126 offset:58368
	s_waitcnt lgkmcnt(8)
	v_mfma_f32_16x16x32_bf16 v[80:83], v[232:235], v[96:99], v[80:83]
	v_cvt_pk_bf16_f32 v0, v64, v65
	v_mfma_f32_16x16x32_bf16 v[76:79], v[236:239], v[96:99], v[76:79]
	v_cvt_pk_bf16_f32 v1, v66, v67
	v_mfma_f32_16x16x32_bf16 v[72:75], v[236:239], v[100:103], v[72:75]
	v_cvt_pk_bf16_f32 v2, v68, v69
	v_mfma_f32_16x16x32_bf16 v[84:87], v[232:235], v[100:103], v[84:87]
	v_cvt_pk_bf16_f32 v3, v70, v71
	ds_read_b128 v[232:235], v126 offset:59392
	ds_read_b128 v[236:239], v126 offset:60416
	s_waitcnt lgkmcnt(6)
	v_mfma_f32_16x16x32_bf16 v[80:83], v[240:243], v[104:107], v[80:83]
	v_cvt_pk_bf16_f32 v4, v56, v57
	v_mfma_f32_16x16x32_bf16 v[76:79], v[244:247], v[104:107], v[76:79]
	v_cvt_pk_bf16_f32 v5, v58, v59
	v_mfma_f32_16x16x32_bf16 v[72:75], v[244:247], v[108:111], v[72:75]
	v_cvt_pk_bf16_f32 v6, v60, v61
	v_mfma_f32_16x16x32_bf16 v[84:87], v[240:243], v[108:111], v[84:87]
	v_cvt_pk_bf16_f32 v7, v62, v63
	ds_read_b128 v[240:243], v126 offset:61440
	ds_read_b128 v[244:247], v126 offset:62464
	s_waitcnt lgkmcnt(6)
	v_mfma_f32_16x16x32_bf16 v[80:83], v[248:251], v[184:187], v[80:83]
	v_pk_max_i16 v0, v0, 0
	v_mfma_f32_16x16x32_bf16 v[76:79], v[252:255], v[184:187], v[76:79]
	v_pk_max_i16 v1, v1, 0
	v_mfma_f32_16x16x32_bf16 v[72:75], v[252:255], v[188:191], v[72:75]
	v_pk_max_i16 v2, v2, 0
	v_mfma_f32_16x16x32_bf16 v[84:87], v[248:251], v[188:191], v[84:87]
	v_pk_max_i16 v3, v3, 0
	ds_read_b128 v[248:251], v126 offset:63488
	ds_read_b128 v[252:255], v126 offset:64512
	s_setprio 0
	s_waitcnt lgkmcnt(6)
	v_mfma_f32_16x16x32_bf16 v[80:83], v[224:227], v[192:195], v[80:83]
	v_pk_max_i16 v4, v4, 0
	v_mfma_f32_16x16x32_bf16 v[76:79], v[228:231], v[192:195], v[76:79]
	v_pk_max_i16 v5, v5, 0
	v_mfma_f32_16x16x32_bf16 v[72:75], v[228:231], v[196:199], v[72:75]
	v_pk_max_i16 v6, v6, 0
	v_mfma_f32_16x16x32_bf16 v[84:87], v[224:227], v[196:199], v[84:87]
	v_pk_max_i16 v7, v7, 0
	s_waitcnt lgkmcnt(4)
	v_mfma_f32_16x16x32_bf16 v[80:83], v[232:235], v[200:203], v[80:83]
	v_mfma_f32_16x16x32_bf16 v[76:79], v[236:239], v[200:203], v[76:79]
	v_mfma_f32_16x16x32_bf16 v[72:75], v[236:239], v[204:207], v[72:75]
	v_mfma_f32_16x16x32_bf16 v[84:87], v[232:235], v[204:207], v[84:87]
.Lnerf_hid_a5:
	s_waitcnt vmcnt(0) lgkmcnt(0)
	s_barrier
	ds_read_b128 v[224:227], v121 offset:8192
	ds_read_b128 v[228:231], v121 offset:9216
	v_mfma_f32_16x16x32_bf16 v[80:83], v[240:243], v[208:211], v[80:83]
	ds_read_b128 v[232:235], v121 offset:10240
	v_mfma_f32_16x16x32_bf16 v[76:79], v[244:247], v[208:211], v[76:79]
	ds_read_b128 v[236:239], v121 offset:11264
	v_mfma_f32_16x16x32_bf16 v[72:75], v[244:247], v[212:215], v[72:75]
	v_mfma_f32_16x16x32_bf16 v[84:87], v[240:243], v[212:215], v[84:87]
	ds_read_b128 v[240:243], v121 offset:12288
	ds_read_b128 v[244:247], v121 offset:13312
	v_mfma_f32_16x16x32_bf16 v[80:83], v[248:251], v[216:219], v[80:83]
	v_mfma_f32_16x16x32_bf16 v[76:79], v[252:255], v[216:219], v[76:79]
	v_mfma_f32_16x16x32_bf16 v[72:75], v[252:255], v[220:223], v[72:75]
	v_mfma_f32_16x16x32_bf16 v[84:87], v[248:251], v[220:223], v[84:87]
	ds_read_b128 v[248:251], v121 offset:14336
	ds_read_b128 v[252:255], v121 offset:15360
	s_setprio 3
	s_waitcnt lgkmcnt(6)
	v_mfma_f32_16x16x32_bf16 v[64:67], v[224:227], v[88:91], v[152:155]
	v_mfma_f32_16x16x32_bf16 v[68:71], v[228:231], v[88:91], v[156:159]
	v_mfma_f32_16x16x32_bf16 v[60:63], v[228:231], v[92:95], v[156:159]
	v_mfma_f32_16x16x32_bf16 v[56:59], v[224:227], v[92:95], v[152:155]
	ds_read_b128 v[224:227], v121 offset:16384
	ds_read_b128 v[228:231], v121 offset:17408
	s_waitcnt lgkmcnt(6)
	ds_read_b128 v[160:163], v183 offset:1408
	ds_read_b128 v[164:167], v183 offset:1472
	v_mfma_f32_16x16x32_bf16 v[64:67], v[232:235], v[96:99], v[64:67]
	v_mfma_f32_16x16x32_bf16 v[68:71], v[236:239], v[96:99], v[68:71]
	s_mov_b32 m0, s28
	s_add_i32 s51, s50, 0x28000
	v_mfma_f32_16x16x32_bf16 v[60:63], v[236:239], v[100:103], v[60:63]
	buffer_load_dwordx4 v125, s[36:39], s51 offen lds
	v_mfma_f32_16x16x32_bf16 v[56:59], v[232:235], v[100:103], v[56:59]
	ds_read_b128 v[232:235], v121 offset:18432
	ds_read_b128 v[236:239], v121 offset:19456
	s_waitcnt lgkmcnt(8)
	v_mfma_f32_16x16x32_bf16 v[64:67], v[240:243], v[104:107], v[64:67]
	v_mfma_f32_16x16x32_bf16 v[68:71], v[244:247], v[104:107], v[68:71]
	s_mov_b32 m0, s29
	s_add_i32 s51, s50, 0x2a000
	v_mfma_f32_16x16x32_bf16 v[60:63], v[244:247], v[108:111], v[60:63]
	buffer_load_dwordx4 v125, s[36:39], s51 offen lds
	v_mfma_f32_16x16x32_bf16 v[56:59], v[240:243], v[108:111], v[56:59]
	ds_read_b128 v[240:243], v121 offset:20480
	ds_read_b128 v[244:247], v121 offset:21504
	s_waitcnt lgkmcnt(8)
	v_mfma_f32_16x16x32_bf16 v[64:67], v[248:251], v[184:187], v[64:67]
	v_mfma_f32_16x16x32_bf16 v[68:71], v[252:255], v[184:187], v[68:71]
	s_mov_b32 m0, s33
	s_add_i32 s51, s50, 0x2c000
	v_mfma_f32_16x16x32_bf16 v[60:63], v[252:255], v[188:191], v[60:63]
	buffer_load_dwordx4 v125, s[36:39], s51 offen lds
	v_mfma_f32_16x16x32_bf16 v[56:59], v[248:251], v[188:191], v[56:59]
	ds_read_b128 v[248:251], v121 offset:22528
	ds_read_b128 v[252:255], v121 offset:23552
	s_setprio 2
	s_waitcnt lgkmcnt(8)
	v_mfma_f32_16x16x32_bf16 v[64:67], v[224:227], v[192:195], v[64:67]
	v_mfma_f32_16x16x32_bf16 v[68:71], v[228:231], v[192:195], v[68:71]
	s_mov_b32 m0, s34
	s_add_i32 s51, s50, 0x2e000
	v_mfma_f32_16x16x32_bf16 v[60:63], v[228:231], v[196:199], v[60:63]
	buffer_load_dwordx4 v125, s[36:39], s51 offen lds
	v_mfma_f32_16x16x32_bf16 v[56:59], v[224:227], v[196:199], v[56:59]
	ds_read_b128 v[224:227], v121 offset:24576
	ds_read_b128 v[228:231], v121 offset:25600
	s_waitcnt lgkmcnt(6)
	v_mfma_f32_16x16x32_bf16 v[64:67], v[232:235], v[200:203], v[64:67]
	v_cvt_pk_bf16_f32 v12, v80, v81
	v_mfma_f32_16x16x32_bf16 v[68:71], v[236:239], v[200:203], v[68:71]
	v_cvt_pk_bf16_f32 v13, v82, v83
	v_mfma_f32_16x16x32_bf16 v[60:63], v[236:239], v[204:207], v[60:63]
	v_cvt_pk_bf16_f32 v14, v76, v77
	v_mfma_f32_16x16x32_bf16 v[56:59], v[232:235], v[204:207], v[56:59]
	v_cvt_pk_bf16_f32 v15, v78, v79
	ds_read_b128 v[232:235], v121 offset:26624
	ds_read_b128 v[236:239], v121 offset:27648
	s_waitcnt lgkmcnt(6)
	ds_read_b128 v[152:155], v183 offset:1536
	ds_read_b128 v[156:159], v183 offset:1600
	v_mfma_f32_16x16x32_bf16 v[64:67], v[240:243], v[208:211], v[64:67]
	v_cvt_pk_bf16_f32 v8, v84, v85
	v_mfma_f32_16x16x32_bf16 v[68:71], v[244:247], v[208:211], v[68:71]
	v_cvt_pk_bf16_f32 v9, v86, v87
	v_mfma_f32_16x16x32_bf16 v[60:63], v[244:247], v[212:215], v[60:63]
	v_cvt_pk_bf16_f32 v10, v72, v73
	v_mfma_f32_16x16x32_bf16 v[56:59], v[240:243], v[212:215], v[56:59]
	v_cvt_pk_bf16_f32 v11, v74, v75
	ds_read_b128 v[240:243], v121 offset:28672
	ds_read_b128 v[244:247], v121 offset:29696
	s_waitcnt lgkmcnt(8)
	v_mfma_f32_16x16x32_bf16 v[64:67], v[248:251], v[216:219], v[64:67]
	v_pk_max_i16 v12, v12, 0
	v_mfma_f32_16x16x32_bf16 v[68:71], v[252:255], v[216:219], v[68:71]
	v_pk_max_i16 v13, v13, 0
	v_mfma_f32_16x16x32_bf16 v[60:63], v[252:255], v[220:223], v[60:63]
	v_pk_max_i16 v14, v14, 0
	v_mfma_f32_16x16x32_bf16 v[56:59], v[248:251], v[220:223], v[56:59]
	v_pk_max_i16 v15, v15, 0
	ds_read_b128 v[248:251], v121 offset:30720
	ds_read_b128 v[252:255], v121 offset:31744
	s_setprio 1
	s_waitcnt lgkmcnt(8)
	v_mfma_f32_16x16x32_bf16 v[80:83], v[224:227], v[88:91], v[160:163]
	v_pk_max_i16 v8, v8, 0
	v_mfma_f32_16x16x32_bf16 v[76:79], v[228:231], v[88:91], v[164:167]
	v_pk_max_i16 v9, v9, 0
	v_mfma_f32_16x16x32_bf16 v[72:75], v[228:231], v[92:95], v[164:167]
	v_pk_max_i16 v10, v10, 0
	v_mfma_f32_16x16x32_bf16 v[84:87], v[224:227], v[92:95], v[160:163]
	v_pk_max_i16 v11, v11, 0
	ds_read_b128 v[224:227], v121 offset:32768
	ds_read_b128 v[228:231], v121 offset:33792
	s_waitcnt lgkmcnt(8)
	v_mfma_f32_16x16x32_bf16 v[80:83], v[232:235], v[96:99], v[80:83]
	v_cvt_pk_bf16_f32 v16, v64, v65
	v_mfma_f32_16x16x32_bf16 v[76:79], v[236:239], v[96:99], v[76:79]
	v_cvt_pk_bf16_f32 v17, v66, v67
	v_mfma_f32_16x16x32_bf16 v[72:75], v[236:239], v[100:103], v[72:75]
	v_cvt_pk_bf16_f32 v18, v68, v69
	v_mfma_f32_16x16x32_bf16 v[84:87], v[232:235], v[100:103], v[84:87]
	v_cvt_pk_bf16_f32 v19, v70, v71
	ds_read_b128 v[232:235], v121 offset:34816
	ds_read_b128 v[236:239], v121 offset:35840
	s_waitcnt lgkmcnt(6)
	v_mfma_f32_16x16x32_bf16 v[80:83], v[240:243], v[104:107], v[80:83]
	v_cvt_pk_bf16_f32 v20, v56, v57
	v_mfma_f32_16x16x32_bf16 v[76:79], v[244:247], v[104:107], v[76:79]
	v_cvt_pk_bf16_f32 v21, v58, v59
	v_mfma_f32_16x16x32_bf16 v[72:75], v[244:247], v[108:111], v[72:75]
	v_cvt_pk_bf16_f32 v22, v60, v61
	v_mfma_f32_16x16x32_bf16 v[84:87], v[240:243], v[108:111], v[84:87]
	v_cvt_pk_bf16_f32 v23, v62, v63
	ds_read_b128 v[240:243], v121 offset:36864
	ds_read_b128 v[244:247], v121 offset:37888
	s_waitcnt lgkmcnt(6)
	v_mfma_f32_16x16x32_bf16 v[80:83], v[248:251], v[184:187], v[80:83]
	v_pk_max_i16 v16, v16, 0
	v_mfma_f32_16x16x32_bf16 v[76:79], v[252:255], v[184:187], v[76:79]
	v_pk_max_i16 v17, v17, 0
	v_mfma_f32_16x16x32_bf16 v[72:75], v[252:255], v[188:191], v[72:75]
	v_pk_max_i16 v18, v18, 0
	v_mfma_f32_16x16x32_bf16 v[84:87], v[248:251], v[188:191], v[84:87]
	v_pk_max_i16 v19, v19, 0
	ds_read_b128 v[248:251], v121 offset:38912
	ds_read_b128 v[252:255], v121 offset:39936
	s_setprio 0
	s_waitcnt lgkmcnt(6)
	v_mfma_f32_16x16x32_bf16 v[80:83], v[224:227], v[192:195], v[80:83]
	v_pk_max_i16 v20, v20, 0
	v_mfma_f32_16x16x32_bf16 v[76:79], v[228:231], v[192:195], v[76:79]
	v_pk_max_i16 v21, v21, 0
	v_mfma_f32_16x16x32_bf16 v[72:75], v[228:231], v[196:199], v[72:75]
	v_pk_max_i16 v22, v22, 0
	v_mfma_f32_16x16x32_bf16 v[84:87], v[224:227], v[196:199], v[84:87]
	v_pk_max_i16 v23, v23, 0
	s_waitcnt lgkmcnt(4)
	v_mfma_f32_16x16x32_bf16 v[80:83], v[232:235], v[200:203], v[80:83]
	v_mfma_f32_16x16x32_bf16 v[76:79], v[236:239], v[200:203], v[76:79]
	v_mfma_f32_16x16x32_bf16 v[72:75], v[236:239], v[204:207], v[72:75]
	v_mfma_f32_16x16x32_bf16 v[84:87], v[232:235], v[204:207], v[84:87]
.Lnerf_hid_a6:
	s_waitcnt vmcnt(0) lgkmcnt(0)
	s_barrier
	ds_read_b128 v[224:227], v121 offset:40960
	ds_read_b128 v[228:231], v121 offset:41984
	v_mfma_f32_16x16x32_bf16 v[80:83], v[240:243], v[208:211], v[80:83]
	ds_read_b128 v[232:235], v121 offset:43008
	v_mfma_f32_16x16x32_bf16 v[76:79], v[244:247], v[208:211], v[76:79]
	ds_read_b128 v[236:239], v121 offset:44032
	v_mfma_f32_16x16x32_bf16 v[72:75], v[244:247], v[212:215], v[72:75]
	v_mfma_f32_16x16x32_bf16 v[84:87], v[240:243], v[212:215], v[84:87]
	ds_read_b128 v[240:243], v121 offset:45056
	ds_read_b128 v[244:247], v121 offset:46080
	v_mfma_f32_16x16x32_bf16 v[80:83], v[248:251], v[216:219], v[80:83]
	v_mfma_f32_16x16x32_bf16 v[76:79], v[252:255], v[216:219], v[76:79]
	v_mfma_f32_16x16x32_bf16 v[72:75], v[252:255], v[220:223], v[72:75]
	v_mfma_f32_16x16x32_bf16 v[84:87], v[248:251], v[220:223], v[84:87]
	ds_read_b128 v[248:251], v121 offset:47104
	ds_read_b128 v[252:255], v121 offset:48128
	s_setprio 3
	s_waitcnt lgkmcnt(6)
	v_mfma_f32_16x16x32_bf16 v[64:67], v[224:227], v[88:91], v[152:155]
	v_mfma_f32_16x16x32_bf16 v[68:71], v[228:231], v[88:91], v[156:159]
	v_mfma_f32_16x16x32_bf16 v[60:63], v[228:231], v[92:95], v[156:159]
	v_mfma_f32_16x16x32_bf16 v[56:59], v[224:227], v[92:95], v[152:155]
	ds_read_b128 v[224:227], v121 offset:49152
	ds_read_b128 v[228:231], v121 offset:50176
	s_waitcnt lgkmcnt(6)
	ds_read_b128 v[160:163], v183 offset:1664
	ds_read_b128 v[164:167], v183 offset:1728
	v_mfma_f32_16x16x32_bf16 v[64:67], v[232:235], v[96:99], v[64:67]
	v_mfma_f32_16x16x32_bf16 v[68:71], v[236:239], v[96:99], v[68:71]
	s_mov_b32 m0, s35
	s_add_i32 s51, s50, 0x30000
	v_mfma_f32_16x16x32_bf16 v[60:63], v[236:239], v[100:103], v[60:63]
	buffer_load_dwordx4 v125, s[36:39], s51 offen lds
	v_mfma_f32_16x16x32_bf16 v[56:59], v[232:235], v[100:103], v[56:59]
	ds_read_b128 v[232:235], v121 offset:51200
	ds_read_b128 v[236:239], v121 offset:52224
	s_waitcnt lgkmcnt(8)
	v_mfma_f32_16x16x32_bf16 v[64:67], v[240:243], v[104:107], v[64:67]
	v_mfma_f32_16x16x32_bf16 v[68:71], v[244:247], v[104:107], v[68:71]
	s_mov_b32 m0, s42
	s_add_i32 s51, s50, 0x32000
	v_mfma_f32_16x16x32_bf16 v[60:63], v[244:247], v[108:111], v[60:63]
	buffer_load_dwordx4 v125, s[36:39], s51 offen lds
	v_mfma_f32_16x16x32_bf16 v[56:59], v[240:243], v[108:111], v[56:59]
	ds_read_b128 v[240:243], v121 offset:53248
	ds_read_b128 v[244:247], v121 offset:54272
	s_waitcnt lgkmcnt(8)
	v_mfma_f32_16x16x32_bf16 v[64:67], v[248:251], v[184:187], v[64:67]
	v_mfma_f32_16x16x32_bf16 v[68:71], v[252:255], v[184:187], v[68:71]
	s_mov_b32 m0, s41
	s_add_i32 s51, s50, 0x34000
	v_mfma_f32_16x16x32_bf16 v[60:63], v[252:255], v[188:191], v[60:63]
	buffer_load_dwordx4 v125, s[36:39], s51 offen lds
	v_mfma_f32_16x16x32_bf16 v[56:59], v[248:251], v[188:191], v[56:59]
	ds_read_b128 v[248:251], v121 offset:55296
	ds_read_b128 v[252:255], v121 offset:56320
	s_setprio 2
	s_waitcnt lgkmcnt(8)
	v_mfma_f32_16x16x32_bf16 v[64:67], v[224:227], v[192:195], v[64:67]
	v_mfma_f32_16x16x32_bf16 v[68:71], v[228:231], v[192:195], v[68:71]
	s_mov_b32 m0, s40
	s_add_i32 s51, s50, 0x36000
	v_mfma_f32_16x16x32_bf16 v[60:63], v[228:231], v[196:199], v[60:63]
	buffer_load_dwordx4 v125, s[36:39], s51 offen lds
	v_mfma_f32_16x16x32_bf16 v[56:59], v[224:227], v[196:199], v[56:59]
	ds_read_b128 v[224:227], v121 offset:57344
	ds_read_b128 v[228:231], v121 offset:58368
	s_waitcnt lgkmcnt(6)
	v_mfma_f32_16x16x32_bf16 v[64:67], v[232:235], v[200:203], v[64:67]
	v_cvt_pk_bf16_f32 v24, v80, v81
	v_mfma_f32_16x16x32_bf16 v[68:71], v[236:239], v[200:203], v[68:71]
	v_cvt_pk_bf16_f32 v25, v82, v83
	v_mfma_f32_16x16x32_bf16 v[60:63], v[236:239], v[204:207], v[60:63]
	v_cvt_pk_bf16_f32 v26, v76, v77
	v_mfma_f32_16x16x32_bf16 v[56:59], v[232:235], v[204:207], v[56:59]
	v_cvt_pk_bf16_f32 v27, v78, v79
	ds_read_b128 v[232:235], v121 offset:59392
	ds_read_b128 v[236:239], v121 offset:60416
	s_waitcnt lgkmcnt(6)
	ds_read_b128 v[152:155], v183 offset:1792
	ds_read_b128 v[156:159], v183 offset:1856
	v_mfma_f32_16x16x32_bf16 v[64:67], v[240:243], v[208:211], v[64:67]
	v_cvt_pk_bf16_f32 v28, v84, v85
	v_mfma_f32_16x16x32_bf16 v[68:71], v[244:247], v[208:211], v[68:71]
	v_cvt_pk_bf16_f32 v29, v86, v87
	v_mfma_f32_16x16x32_bf16 v[60:63], v[244:247], v[212:215], v[60:63]
	v_cvt_pk_bf16_f32 v30, v72, v73
	v_mfma_f32_16x16x32_bf16 v[56:59], v[240:243], v[212:215], v[56:59]
	v_cvt_pk_bf16_f32 v31, v74, v75
	ds_read_b128 v[240:243], v121 offset:61440
	ds_read_b128 v[244:247], v121 offset:62464
	s_waitcnt lgkmcnt(8)
	v_mfma_f32_16x16x32_bf16 v[64:67], v[248:251], v[216:219], v[64:67]
	v_pk_max_i16 v24, v24, 0
	v_mfma_f32_16x16x32_bf16 v[68:71], v[252:255], v[216:219], v[68:71]
	v_pk_max_i16 v25, v25, 0
	v_mfma_f32_16x16x32_bf16 v[60:63], v[252:255], v[220:223], v[60:63]
	v_pk_max_i16 v26, v26, 0
	v_mfma_f32_16x16x32_bf16 v[56:59], v[248:251], v[220:223], v[56:59]
	v_pk_max_i16 v27, v27, 0
	ds_read_b128 v[248:251], v121 offset:63488
	ds_read_b128 v[252:255], v121 offset:64512
	s_setprio 1
	s_waitcnt lgkmcnt(8)
	v_mfma_f32_16x16x32_bf16 v[80:83], v[224:227], v[88:91], v[160:163]
	v_pk_max_i16 v28, v28, 0
	v_mfma_f32_16x16x32_bf16 v[76:79], v[228:231], v[88:91], v[164:167]
	v_pk_max_i16 v29, v29, 0
	v_mfma_f32_16x16x32_bf16 v[72:75], v[228:231], v[92:95], v[164:167]
	v_pk_max_i16 v30, v30, 0
	v_mfma_f32_16x16x32_bf16 v[84:87], v[224:227], v[92:95], v[160:163]
	v_pk_max_i16 v31, v31, 0
	ds_read_b128 v[224:227], v126 offset:57344
	ds_read_b128 v[228:231], v126 offset:58368
	s_waitcnt lgkmcnt(8)
	v_mfma_f32_16x16x32_bf16 v[80:83], v[232:235], v[96:99], v[80:83]
	v_cvt_pk_bf16_f32 v32, v64, v65
	v_mfma_f32_16x16x32_bf16 v[76:79], v[236:239], v[96:99], v[76:79]
	v_cvt_pk_bf16_f32 v33, v66, v67
	v_mfma_f32_16x16x32_bf16 v[72:75], v[236:239], v[100:103], v[72:75]
	v_cvt_pk_bf16_f32 v34, v68, v69
	v_mfma_f32_16x16x32_bf16 v[84:87], v[232:235], v[100:103], v[84:87]
	v_cvt_pk_bf16_f32 v35, v70, v71
	ds_read_b128 v[232:235], v126 offset:59392
	ds_read_b128 v[236:239], v126 offset:60416
	s_waitcnt lgkmcnt(6)
	v_mfma_f32_16x16x32_bf16 v[80:83], v[240:243], v[104:107], v[80:83]
	v_cvt_pk_bf16_f32 v36, v56, v57
	v_mfma_f32_16x16x32_bf16 v[76:79], v[244:247], v[104:107], v[76:79]
	v_cvt_pk_bf16_f32 v37, v58, v59
	v_mfma_f32_16x16x32_bf16 v[72:75], v[244:247], v[108:111], v[72:75]
	v_cvt_pk_bf16_f32 v38, v60, v61
	v_mfma_f32_16x16x32_bf16 v[84:87], v[240:243], v[108:111], v[84:87]
	v_cvt_pk_bf16_f32 v39, v62, v63
	ds_read_b128 v[240:243], v126 offset:61440
	ds_read_b128 v[244:247], v126 offset:62464
	s_waitcnt lgkmcnt(6)
	v_mfma_f32_16x16x32_bf16 v[80:83], v[248:251], v[184:187], v[80:83]
	v_pk_max_i16 v32, v32, 0
	v_mfma_f32_16x16x32_bf16 v[76:79], v[252:255], v[184:187], v[76:79]
	v_pk_max_i16 v33, v33, 0
	v_mfma_f32_16x16x32_bf16 v[72:75], v[252:255], v[188:191], v[72:75]
	v_pk_max_i16 v34, v34, 0
	v_mfma_f32_16x16x32_bf16 v[84:87], v[248:251], v[188:191], v[84:87]
	v_pk_max_i16 v35, v35, 0
	ds_read_b128 v[248:251], v126 offset:63488
	ds_read_b128 v[252:255], v126 offset:64512
	s_setprio 0
	s_waitcnt lgkmcnt(6)
	v_mfma_f32_16x16x32_bf16 v[80:83], v[224:227], v[192:195], v[80:83]
	v_pk_max_i16 v36, v36, 0
	v_mfma_f32_16x16x32_bf16 v[76:79], v[228:231], v[192:195], v[76:79]
	v_pk_max_i16 v37, v37, 0
	v_mfma_f32_16x16x32_bf16 v[72:75], v[228:231], v[196:199], v[72:75]
	v_pk_max_i16 v38, v38, 0
	v_mfma_f32_16x16x32_bf16 v[84:87], v[224:227], v[196:199], v[84:87]
	v_pk_max_i16 v39, v39, 0
	s_waitcnt lgkmcnt(4)
	v_mfma_f32_16x16x32_bf16 v[80:83], v[232:235], v[200:203], v[80:83]
	v_mfma_f32_16x16x32_bf16 v[76:79], v[236:239], v[200:203], v[76:79]
	v_mfma_f32_16x16x32_bf16 v[72:75], v[236:239], v[204:207], v[72:75]
	v_mfma_f32_16x16x32_bf16 v[84:87], v[232:235], v[204:207], v[84:87]
.Lnerf_hid_a7:
	s_waitcnt vmcnt(0) lgkmcnt(0)
	s_barrier
	ds_read_b128 v[224:227], v121 offset:8192
	ds_read_b128 v[228:231], v121 offset:9216
	v_mfma_f32_16x16x32_bf16 v[80:83], v[240:243], v[208:211], v[80:83]
	ds_read_b128 v[232:235], v121 offset:10240
	v_mfma_f32_16x16x32_bf16 v[76:79], v[244:247], v[208:211], v[76:79]
	ds_read_b128 v[236:239], v121 offset:11264
	v_mfma_f32_16x16x32_bf16 v[72:75], v[244:247], v[212:215], v[72:75]
	v_mfma_f32_16x16x32_bf16 v[84:87], v[240:243], v[212:215], v[84:87]
	ds_read_b128 v[240:243], v121 offset:12288
	ds_read_b128 v[244:247], v121 offset:13312
	v_mfma_f32_16x16x32_bf16 v[80:83], v[248:251], v[216:219], v[80:83]
	v_mfma_f32_16x16x32_bf16 v[76:79], v[252:255], v[216:219], v[76:79]
	v_mfma_f32_16x16x32_bf16 v[72:75], v[252:255], v[220:223], v[72:75]
	v_mfma_f32_16x16x32_bf16 v[84:87], v[248:251], v[220:223], v[84:87]
	ds_read_b128 v[248:251], v121 offset:14336
	ds_read_b128 v[252:255], v121 offset:15360
	s_setprio 3
	s_waitcnt lgkmcnt(6)
	v_mfma_f32_16x16x32_bf16 v[64:67], v[224:227], v[88:91], v[152:155]
	v_mfma_f32_16x16x32_bf16 v[68:71], v[228:231], v[88:91], v[156:159]
	v_mfma_f32_16x16x32_bf16 v[60:63], v[228:231], v[92:95], v[156:159]
	v_mfma_f32_16x16x32_bf16 v[56:59], v[224:227], v[92:95], v[152:155]
	ds_read_b128 v[224:227], v121 offset:16384
	ds_read_b128 v[228:231], v121 offset:17408
	s_waitcnt lgkmcnt(6)
	ds_read_b128 v[160:163], v183 offset:1920
	ds_read_b128 v[164:167], v183 offset:1984
	v_mfma_f32_16x16x32_bf16 v[64:67], v[232:235], v[96:99], v[64:67]
	v_mfma_f32_16x16x32_bf16 v[68:71], v[236:239], v[96:99], v[68:71]
	s_mov_b32 m0, s28
	s_add_i32 s51, s50, 0x38000
	v_mfma_f32_16x16x32_bf16 v[60:63], v[236:239], v[100:103], v[60:63]
	buffer_load_dwordx4 v125, s[36:39], s51 offen lds
	v_mfma_f32_16x16x32_bf16 v[56:59], v[232:235], v[100:103], v[56:59]
	ds_read_b128 v[232:235], v121 offset:18432
	ds_read_b128 v[236:239], v121 offset:19456
	s_waitcnt lgkmcnt(8)
	v_mfma_f32_16x16x32_bf16 v[64:67], v[240:243], v[104:107], v[64:67]
	v_mfma_f32_16x16x32_bf16 v[68:71], v[244:247], v[104:107], v[68:71]
	s_mov_b32 m0, s29
	s_add_i32 s51, s50, 0x3a000
	v_mfma_f32_16x16x32_bf16 v[60:63], v[244:247], v[108:111], v[60:63]
	buffer_load_dwordx4 v125, s[36:39], s51 offen lds
	v_mfma_f32_16x16x32_bf16 v[56:59], v[240:243], v[108:111], v[56:59]
	ds_read_b128 v[240:243], v121 offset:20480
	ds_read_b128 v[244:247], v121 offset:21504
	s_waitcnt lgkmcnt(8)
	v_mfma_f32_16x16x32_bf16 v[64:67], v[248:251], v[184:187], v[64:67]
	v_mfma_f32_16x16x32_bf16 v[68:71], v[252:255], v[184:187], v[68:71]
	s_mov_b32 m0, s33
	s_add_i32 s51, s50, 0x3c000
	v_mfma_f32_16x16x32_bf16 v[60:63], v[252:255], v[188:191], v[60:63]
	buffer_load_dwordx4 v125, s[36:39], s51 offen lds
	v_mfma_f32_16x16x32_bf16 v[56:59], v[248:251], v[188:191], v[56:59]
	ds_read_b128 v[248:251], v121 offset:22528
	ds_read_b128 v[252:255], v121 offset:23552
	s_setprio 2
	s_waitcnt lgkmcnt(8)
	v_mfma_f32_16x16x32_bf16 v[64:67], v[224:227], v[192:195], v[64:67]
	v_mfma_f32_16x16x32_bf16 v[68:71], v[228:231], v[192:195], v[68:71]
	s_mov_b32 m0, s34
	s_add_i32 s51, s50, 0x3e000
	v_mfma_f32_16x16x32_bf16 v[60:63], v[228:231], v[196:199], v[60:63]
	buffer_load_dwordx4 v125, s[36:39], s51 offen lds
	v_mfma_f32_16x16x32_bf16 v[56:59], v[224:227], v[196:199], v[56:59]
	ds_read_b128 v[224:227], v121 offset:24576
	ds_read_b128 v[228:231], v121 offset:25600
	s_waitcnt lgkmcnt(6)
	v_mfma_f32_16x16x32_bf16 v[64:67], v[232:235], v[200:203], v[64:67]
	v_cvt_pk_bf16_f32 v40, v80, v81
	v_mfma_f32_16x16x32_bf16 v[68:71], v[236:239], v[200:203], v[68:71]
	v_cvt_pk_bf16_f32 v41, v82, v83
	v_mfma_f32_16x16x32_bf16 v[60:63], v[236:239], v[204:207], v[60:63]
	v_cvt_pk_bf16_f32 v42, v76, v77
	v_mfma_f32_16x16x32_bf16 v[56:59], v[232:235], v[204:207], v[56:59]
	v_cvt_pk_bf16_f32 v43, v78, v79
	ds_read_b128 v[232:235], v121 offset:26624
	ds_read_b128 v[236:239], v121 offset:27648
	s_waitcnt lgkmcnt(6)
	ds_read_b128 v[152:155], v183 offset:2048
	ds_read_b128 v[156:159], v183 offset:2112
	v_mfma_f32_16x16x32_bf16 v[64:67], v[240:243], v[208:211], v[64:67]
	v_cvt_pk_bf16_f32 v44, v84, v85
	v_mfma_f32_16x16x32_bf16 v[68:71], v[244:247], v[208:211], v[68:71]
	v_cvt_pk_bf16_f32 v45, v86, v87
	v_mfma_f32_16x16x32_bf16 v[60:63], v[244:247], v[212:215], v[60:63]
	v_cvt_pk_bf16_f32 v46, v72, v73
	v_mfma_f32_16x16x32_bf16 v[56:59], v[240:243], v[212:215], v[56:59]
	v_cvt_pk_bf16_f32 v47, v74, v75
	ds_read_b128 v[240:243], v121 offset:28672
	ds_read_b128 v[244:247], v121 offset:29696
	s_waitcnt lgkmcnt(8)
	v_mfma_f32_16x16x32_bf16 v[64:67], v[248:251], v[216:219], v[64:67]
	v_pk_max_i16 v40, v40, 0
	v_mfma_f32_16x16x32_bf16 v[68:71], v[252:255], v[216:219], v[68:71]
	v_pk_max_i16 v41, v41, 0
	v_mfma_f32_16x16x32_bf16 v[60:63], v[252:255], v[220:223], v[60:63]
	v_pk_max_i16 v42, v42, 0
	v_mfma_f32_16x16x32_bf16 v[56:59], v[248:251], v[220:223], v[56:59]
	v_pk_max_i16 v43, v43, 0
	ds_read_b128 v[248:251], v121 offset:30720
	ds_read_b128 v[252:255], v121 offset:31744
	s_setprio 1
	s_waitcnt lgkmcnt(8)
	v_mfma_f32_16x16x32_bf16 v[80:83], v[224:227], v[88:91], v[160:163]
	v_pk_max_i16 v44, v44, 0
	v_mfma_f32_16x16x32_bf16 v[76:79], v[228:231], v[88:91], v[164:167]
	v_pk_max_i16 v45, v45, 0
	v_mfma_f32_16x16x32_bf16 v[72:75], v[228:231], v[92:95], v[164:167]
	v_pk_max_i16 v46, v46, 0
	v_mfma_f32_16x16x32_bf16 v[84:87], v[224:227], v[92:95], v[160:163]
	v_pk_max_i16 v47, v47, 0
	ds_read_b128 v[224:227], v121 offset:32768
	ds_read_b128 v[228:231], v121 offset:33792
	s_waitcnt lgkmcnt(8)
	v_mfma_f32_16x16x32_bf16 v[80:83], v[232:235], v[96:99], v[80:83]
	v_cvt_pk_bf16_f32 v48, v64, v65
	v_mfma_f32_16x16x32_bf16 v[76:79], v[236:239], v[96:99], v[76:79]
	v_cvt_pk_bf16_f32 v49, v66, v67
	v_mfma_f32_16x16x32_bf16 v[72:75], v[236:239], v[100:103], v[72:75]
	v_cvt_pk_bf16_f32 v50, v68, v69
	v_mfma_f32_16x16x32_bf16 v[84:87], v[232:235], v[100:103], v[84:87]
	v_cvt_pk_bf16_f32 v51, v70, v71
	ds_read_b128 v[232:235], v121 offset:34816
	ds_read_b128 v[236:239], v121 offset:35840
	s_waitcnt lgkmcnt(6)
	v_mfma_f32_16x16x32_bf16 v[80:83], v[240:243], v[104:107], v[80:83]
	v_cvt_pk_bf16_f32 v52, v56, v57
	v_mfma_f32_16x16x32_bf16 v[76:79], v[244:247], v[104:107], v[76:79]
	v_cvt_pk_bf16_f32 v53, v58, v59
	v_mfma_f32_16x16x32_bf16 v[72:75], v[244:247], v[108:111], v[72:75]
	v_cvt_pk_bf16_f32 v54, v60, v61
	v_mfma_f32_16x16x32_bf16 v[84:87], v[240:243], v[108:111], v[84:87]
	v_cvt_pk_bf16_f32 v55, v62, v63
	ds_read_b128 v[240:243], v121 offset:36864
	ds_read_b128 v[244:247], v121 offset:37888
	s_waitcnt lgkmcnt(6)
	v_mfma_f32_16x16x32_bf16 v[80:83], v[248:251], v[184:187], v[80:83]
	v_pk_max_i16 v48, v48, 0
	v_mfma_f32_16x16x32_bf16 v[76:79], v[252:255], v[184:187], v[76:79]
	v_pk_max_i16 v49, v49, 0
	v_mfma_f32_16x16x32_bf16 v[72:75], v[252:255], v[188:191], v[72:75]
	v_pk_max_i16 v50, v50, 0
	v_mfma_f32_16x16x32_bf16 v[84:87], v[248:251], v[188:191], v[84:87]
	v_pk_max_i16 v51, v51, 0
	ds_read_b128 v[248:251], v121 offset:38912
	ds_read_b128 v[252:255], v121 offset:39936
	s_setprio 0
	s_waitcnt lgkmcnt(6)
	v_mfma_f32_16x16x32_bf16 v[80:83], v[224:227], v[192:195], v[80:83]
	v_pk_max_i16 v52, v52, 0
	v_mfma_f32_16x16x32_bf16 v[76:79], v[228:231], v[192:195], v[76:79]
	v_pk_max_i16 v53, v53, 0
	v_mfma_f32_16x16x32_bf16 v[72:75], v[228:231], v[196:199], v[72:75]
	v_pk_max_i16 v54, v54, 0
	v_mfma_f32_16x16x32_bf16 v[84:87], v[224:227], v[196:199], v[84:87]
	v_pk_max_i16 v55, v55, 0
	s_waitcnt lgkmcnt(4)
	v_mfma_f32_16x16x32_bf16 v[80:83], v[232:235], v[200:203], v[80:83]
	v_mfma_f32_16x16x32_bf16 v[76:79], v[236:239], v[200:203], v[76:79]
	v_mfma_f32_16x16x32_bf16 v[72:75], v[236:239], v[204:207], v[72:75]
	v_mfma_f32_16x16x32_bf16 v[84:87], v[232:235], v[204:207], v[84:87]
	s_add_i32 s50, s50, 0x40000
	v_add_u32_e32 v183, 0x800, v183
	s_add_i32 s52, s52, 1
	s_branch .Lnerf_hid_a0

.Lnerf_head:
	s_waitcnt vmcnt(0) lgkmcnt(0)
	s_barrier
	ds_read_b128 v[224:227], v121 offset:40960
	ds_read_b128 v[228:231], v121 offset:41984
	ds_read_b128 v[4:7], v183 offset:1024
	ds_read_b128 v[0:3], v183 offset:1024
	v_mfma_f32_16x16x32_bf16 v[80:83], v[240:243], v[48:51], v[80:83]
	ds_read_b128 v[232:235], v121 offset:43008
	v_mfma_f32_16x16x32_bf16 v[76:79], v[244:247], v[48:51], v[76:79]
	ds_read_b128 v[236:239], v121 offset:44032
	v_mfma_f32_16x16x32_bf16 v[72:75], v[244:247], v[52:55], v[72:75]
	v_mfma_f32_16x16x32_bf16 v[84:87], v[240:243], v[52:55], v[84:87]
	ds_read_b128 v[240:243], v121 offset:45056
	ds_read_b128 v[244:247], v121 offset:46080
	v_mfma_f32_16x16x32_bf16 v[80:83], v[248:251], v[112:115], v[80:83]
	v_mfma_f32_16x16x32_bf16 v[76:79], v[252:255], v[112:115], v[76:79]
	v_mfma_f32_16x16x32_bf16 v[72:75], v[252:255], v[116:119], v[72:75]
	v_mfma_f32_16x16x32_bf16 v[84:87], v[248:251], v[116:119], v[84:87]
	ds_read_b128 v[248:251], v121 offset:47104
	ds_read_b128 v[252:255], v121 offset:48128
	s_waitcnt lgkmcnt(7)
	v_mfma_f32_16x16x32_bf16 v[4:7], v[224:227], v[88:91], v[4:7]
	s_waitcnt lgkmcnt(6)
	v_mfma_f32_16x16x32_bf16 v[0:3], v[224:227], v[92:95], v[0:3]
	v_cvt_pk_bf16_f32 v216, v80, v81
	v_cvt_pk_bf16_f32 v217, v82, v83
	v_mfma_f32_16x16x32_bf16 v[4:7], v[228:231], v[96:99], v[4:7]
	v_cvt_pk_bf16_f32 v218, v76, v77
	v_cvt_pk_bf16_f32 v219, v78, v79
	v_mfma_f32_16x16x32_bf16 v[0:3], v[228:231], v[100:103], v[0:3]
	v_cvt_pk_bf16_f32 v220, v84, v85
	v_cvt_pk_bf16_f32 v221, v86, v87
	s_waitcnt lgkmcnt(5)
	v_mfma_f32_16x16x32_bf16 v[4:7], v[232:235], v[104:107], v[4:7]
	v_cvt_pk_bf16_f32 v222, v72, v73
	v_cvt_pk_bf16_f32 v223, v74, v75
	v_mfma_f32_16x16x32_bf16 v[0:3], v[232:235], v[108:111], v[0:3]
	v_pk_max_i16 v216, v216, 0
	v_pk_max_i16 v217, v217, 0
	s_waitcnt lgkmcnt(4)
	v_mfma_f32_16x16x32_bf16 v[4:7], v[236:239], v[184:187], v[4:7]
	v_pk_max_i16 v218, v218, 0
	v_pk_max_i16 v219, v219, 0
	v_mfma_f32_16x16x32_bf16 v[0:3], v[236:239], v[188:191], v[0:3]
	v_pk_max_i16 v220, v220, 0
	v_pk_max_i16 v221, v221, 0
	s_waitcnt lgkmcnt(3)
	v_mfma_f32_16x16x32_bf16 v[4:7], v[240:243], v[192:195], v[4:7]
	v_pk_max_i16 v222, v222, 0
	v_pk_max_i16 v223, v223, 0
	v_mfma_f32_16x16x32_bf16 v[0:3], v[240:243], v[196:199], v[0:3]
	s_waitcnt lgkmcnt(2)
	v_mfma_f32_16x16x32_bf16 v[4:7], v[244:247], v[200:203], v[4:7]
	v_mfma_f32_16x16x32_bf16 v[0:3], v[244:247], v[204:207], v[0:3]
	s_waitcnt lgkmcnt(1)
	v_mfma_f32_16x16x32_bf16 v[4:7], v[248:251], v[208:211], v[4:7]
	v_mfma_f32_16x16x32_bf16 v[0:3], v[248:251], v[212:215], v[0:3]
	s_nop 1
	s_waitcnt lgkmcnt(0)
	v_mfma_f32_16x16x32_bf16 v[4:7], v[252:255], v[216:219], v[4:7]
	v_mfma_f32_16x16x32_bf16 v[0:3], v[252:255], v[220:223], v[0:3]
	s_nop 7
	s_nop 1
	s_setprio 0
	s_and_saveexec_b64 s[20:21], s[2:3]
	s_cbranch_execz .LBB1_20
	s_nop 4
	v_mul_f32_e32 v6, 0xbfb8aa3b, v6
	v_mul_f32_e32 v7, 0xbfb8aa3b, v7
	v_mul_f32_e32 v4, 0xbfb8aa3b, v4
	v_mul_f32_e32 v5, 0xbfb8aa3b, v5
	v_exp_f32_e32 v6, v6
	v_exp_f32_e32 v7, v7
	v_exp_f32_e32 v4, v4
	v_exp_f32_e32 v5, v5
	s_lshl_b32 s24, s45, 6
	s_add_i32 s47, s43, s24
	s_nop 0
	v_add_f32_e32 v6, 1.0, v6
	v_add_f32_e32 v7, 1.0, v7
	v_add_f32_e32 v4, 1.0, v4
	v_add_f32_e32 v5, 1.0, v5
	v_rcp_f32_e32 v6, v6
	v_rcp_f32_e32 v7, v7
	v_rcp_f32_e32 v4, v4
	v_rcp_f32_e32 v5, v5
	s_mov_b64 s[24:25], -1
	s_nop 0
	s_and_b64 vcc, exec, s[16:17]
	s_cbranch_vccz .LBB1_14
	v_or_b32_e32 v8, s47, v130
	v_lshl_add_u32 v8, v8, 4, v182
	ds_write_b128 v8, v[4:7]
	s_mov_b64 s[24:25], 0

.LBB1_16:
	v_mul_f32_e32 v2, 0xbfb8aa3b, v2
	v_mul_f32_e32 v3, 0xbfb8aa3b, v3
	v_mul_f32_e32 v0, 0xbfb8aa3b, v0
	v_mul_f32_e32 v1, 0xbfb8aa3b, v1
	v_exp_f32_e32 v2, v2
	v_exp_f32_e32 v3, v3
	v_exp_f32_e32 v0, v0
	v_exp_f32_e32 v1, v1
	s_nop 0
	v_add_f32_e32 v2, 1.0, v2
	v_add_f32_e32 v3, 1.0, v3
	v_add_f32_e32 v0, 1.0, v0
	v_add_f32_e32 v1, 1.0, v1
	v_rcp_f32_e32 v2, v2
	v_rcp_f32_e32 v3, v3
	v_rcp_f32_e32 v0, v0
	v_rcp_f32_e32 v1, v1
	s_nop 0
	s_and_b64 vcc, exec, s[8:9]
	s_mov_b64 s[8:9], -1
	s_cbranch_vccnz .LBB1_18
	v_or_b32_e32 v4, s47, v138
	v_lshl_add_u32 v4, v4, 4, v182
	s_mov_b64 s[8:9], 0
	ds_write_b128 v4, v[0:3]
